# dead zero-init elimination: v_mov vN,0 in front of v_cvt_pk_fp8 low+high pairs removed (cv loops, MoE epilogues, rowpass G)
# speedup vs baseline: 1.0024x; 1.0020x over previous
.LBB0_580:
	s_waitcnt vmcnt(15)
	v_mul_f32_e32 v0, 0x42800000, v2
	s_waitcnt vmcnt(14)
	v_mul_f32_e32 v131, 0x42800000, v6
	v_cvt_pk_fp8_f32 v130, v0, v131
	s_waitcnt vmcnt(13)
	v_mul_f32_e32 v132, 0x42800000, v10
	s_waitcnt vmcnt(12)
	v_mul_f32_e32 v133, 0x42800000, v14
	s_waitcnt vmcnt(11)
	v_mul_f32_e32 v0, 0x42800000, v18
	v_cvt_pk_fp8_f32 v130, v132, v133 op_sel:[0,0,1]
	s_waitcnt vmcnt(10)
	v_mul_f32_e32 v132, 0x42800000, v22
	v_cvt_pk_fp8_f32 v131, v0, v132
	s_waitcnt vmcnt(9)
	v_mul_f32_e32 v133, 0x42800000, v26
	s_waitcnt vmcnt(8)
	v_mul_f32_e32 v138, 0x42800000, v30
	s_waitcnt vmcnt(7)
	v_mul_f32_e32 v0, 0x42800000, v34
	v_cvt_pk_fp8_f32 v131, v133, v138 op_sel:[0,0,1]
	s_waitcnt vmcnt(6)
	v_mul_f32_e32 v133, 0x42800000, v38
	v_cvt_pk_fp8_f32 v132, v0, v133
	s_waitcnt vmcnt(5)
	v_mul_f32_e32 v138, 0x42800000, v42
	s_waitcnt vmcnt(4)
	v_mul_f32_e32 v139, 0x42800000, v46
	s_waitcnt vmcnt(3)
	v_mul_f32_e32 v0, 0x42800000, v50
	v_cvt_pk_fp8_f32 v132, v138, v139 op_sel:[0,0,1]
	s_waitcnt vmcnt(2)
	v_mul_f32_e32 v138, 0x42800000, v54
	v_cvt_pk_fp8_f32 v133, v0, v138
	s_waitcnt vmcnt(1)
	v_mul_f32_e32 v139, 0x42800000, v58
	s_waitcnt vmcnt(0)
	v_mul_f32_e32 v149, 0x42800000, v62
	v_mul_f32_e32 v0, 0x42800000, v3
	v_cvt_pk_fp8_f32 v133, v139, v149 op_sel:[0,0,1]
	v_mul_f32_e32 v138, 0x42800000, v31
	v_mul_f32_e32 v139, 0x42800000, v47
	v_mul_f32_e32 v149, 0x42800000, v63
	ds_write_b128 v144, v[130:133]
	v_mul_f32_e32 v131, 0x42800000, v7
	s_nop 0
	v_cvt_pk_fp8_f32 v130, v0, v131
	v_mul_f32_e32 v132, 0x42800000, v11
	v_mul_f32_e32 v133, 0x42800000, v15
	v_mul_f32_e32 v0, 0x42800000, v19
	v_cvt_pk_fp8_f32 v130, v132, v133 op_sel:[0,0,1]
	v_mul_f32_e32 v132, 0x42800000, v23
	v_cvt_pk_fp8_f32 v131, v0, v132
	v_mul_f32_e32 v133, 0x42800000, v27
	v_mul_f32_e32 v0, 0x42800000, v35
	v_cvt_pk_fp8_f32 v131, v133, v138 op_sel:[0,0,1]
	v_mul_f32_e32 v133, 0x42800000, v39
	v_cvt_pk_fp8_f32 v132, v0, v133
	v_mul_f32_e32 v138, 0x42800000, v43
	v_mul_f32_e32 v0, 0x42800000, v51
	v_cvt_pk_fp8_f32 v132, v138, v139 op_sel:[0,0,1]
	v_mul_f32_e32 v138, 0x42800000, v55
	v_cvt_pk_fp8_f32 v133, v0, v138
	v_mul_f32_e32 v139, 0x42800000, v59
	v_mul_f32_e32 v0, 0x42800000, v4
	v_mul_f32_e32 v138, 0x42800000, v32
	v_cvt_pk_fp8_f32 v133, v139, v149 op_sel:[0,0,1]
	v_mul_f32_e32 v139, 0x42800000, v48
	v_mul_f32_e32 v149, 0x42800000, v64
	s_cmp_lg_u32 s31, 0
	ds_write_b128 v144, v[130:133] offset:128
	v_mul_f32_e32 v131, 0x42800000, v8
	s_nop 0
	v_cvt_pk_fp8_f32 v130, v0, v131
	v_mul_f32_e32 v132, 0x42800000, v12
	v_mul_f32_e32 v133, 0x42800000, v16
	v_mul_f32_e32 v0, 0x42800000, v20
	v_cvt_pk_fp8_f32 v130, v132, v133 op_sel:[0,0,1]
	v_mul_f32_e32 v132, 0x42800000, v24
	v_cvt_pk_fp8_f32 v131, v0, v132
	v_mul_f32_e32 v133, 0x42800000, v28
	v_mul_f32_e32 v0, 0x42800000, v36
	v_cvt_pk_fp8_f32 v131, v133, v138 op_sel:[0,0,1]
	v_mul_f32_e32 v133, 0x42800000, v40
	v_cvt_pk_fp8_f32 v132, v0, v133
	v_mul_f32_e32 v138, 0x42800000, v44
	v_mul_f32_e32 v0, 0x42800000, v52
	v_cvt_pk_fp8_f32 v132, v138, v139 op_sel:[0,0,1]
	v_mul_f32_e32 v138, 0x42800000, v56
	v_cvt_pk_fp8_f32 v133, v0, v138
	v_mul_f32_e32 v139, 0x42800000, v60
	v_mul_f32_e32 v0, 0x42800000, v5
	v_mul_f32_e32 v138, 0x42800000, v33
	v_cvt_pk_fp8_f32 v133, v139, v149 op_sel:[0,0,1]
	v_mul_f32_e32 v139, 0x42800000, v49
	v_mul_f32_e32 v149, 0x42800000, v65
	s_cselect_b64 s[20:21], -1, 0
	ds_write_b128 v144, v[130:133] offset:256
	v_mul_f32_e32 v131, 0x42800000, v9
	s_nop 0
	v_cvt_pk_fp8_f32 v130, v0, v131
	v_mul_f32_e32 v132, 0x42800000, v13
	v_mul_f32_e32 v133, 0x42800000, v17
	v_mul_f32_e32 v0, 0x42800000, v21
	v_cvt_pk_fp8_f32 v130, v132, v133 op_sel:[0,0,1]
	v_mul_f32_e32 v132, 0x42800000, v25
	v_cvt_pk_fp8_f32 v131, v0, v132
	v_mul_f32_e32 v133, 0x42800000, v29
	v_mul_f32_e32 v0, 0x42800000, v37
	v_cvt_pk_fp8_f32 v131, v133, v138 op_sel:[0,0,1]
	v_mul_f32_e32 v133, 0x42800000, v41
	v_cvt_pk_fp8_f32 v132, v0, v133
	v_mul_f32_e32 v138, 0x42800000, v45
	v_mul_f32_e32 v0, 0x42800000, v53
	v_cvt_pk_fp8_f32 v132, v138, v139 op_sel:[0,0,1]
	v_mul_f32_e32 v138, 0x42800000, v57
	v_cvt_pk_fp8_f32 v133, v0, v138
	v_mul_f32_e32 v139, 0x42800000, v61
	v_add_u32_e32 v138, s8, v140
	s_cmp_eq_u32 s31, 0
	v_cvt_pk_fp8_f32 v133, v139, v149 op_sel:[0,0,1]
	ds_write_b128 v144, v[130:133] offset:384
	s_waitcnt lgkmcnt(0)
	s_barrier
	ds_read_b128 v[130:133], v145
	s_cbranch_scc1 .LBB0_586
	v_cmp_lt_i32_e32 vcc, s47, v138
	v_lshlrev_b32_e32 v0, 1, v138
	v_and_b32_e32 v139, 0x7f, v138
	s_and_saveexec_b64 s[6:7], vcc
	s_xor_b64 s[6:7], exec, s[6:7]
	v_add_u32_e32 v0, 0x7ffff800, v0
	v_and_b32_e32 v0, 0x7fffff00, v0
	v_or3_b32 v138, v139, v0, s64
	s_andn2_saveexec_b64 s[6:7], s[6:7]
	v_and_or_b32 v138, v0, s65, v139
	s_or_b64 exec, exec, s[6:7]

.LBB0_612:
	v_mul_f32_e32 v0, 0x42800000, v70
	v_mul_f32_e32 v131, 0x42800000, v66
	s_nop 0
	v_cvt_pk_fp8_f32 v130, v0, v131
	v_mul_f32_e32 v132, 0x42800000, v78
	v_mul_f32_e32 v133, 0x42800000, v74
	v_mul_f32_e32 v0, 0x42800000, v86
	v_cvt_pk_fp8_f32 v130, v132, v133 op_sel:[0,0,1]
	v_mul_f32_e32 v132, 0x42800000, v82
	v_cvt_pk_fp8_f32 v131, v0, v132
	v_mul_f32_e32 v133, 0x42800000, v94
	v_mul_f32_e32 v138, 0x42800000, v90
	v_mul_f32_e32 v0, 0x42800000, v98
	v_cvt_pk_fp8_f32 v131, v133, v138 op_sel:[0,0,1]
	v_mul_f32_e32 v133, 0x42800000, v102
	v_cvt_pk_fp8_f32 v132, v0, v133
	v_mul_f32_e32 v138, 0x42800000, v106
	v_mul_f32_e32 v139, 0x42800000, v110
	v_mul_f32_e32 v0, 0x42800000, v114
	v_cvt_pk_fp8_f32 v132, v138, v139 op_sel:[0,0,1]
	v_mul_f32_e32 v138, 0x42800000, v118
	v_cvt_pk_fp8_f32 v133, v0, v138
	v_mul_f32_e32 v139, 0x42800000, v122
	v_mul_f32_e32 v149, 0x42800000, v126
	v_mul_f32_e32 v0, 0x42800000, v71
	v_cvt_pk_fp8_f32 v133, v139, v149 op_sel:[0,0,1]
	v_mul_f32_e32 v138, 0x42800000, v91
	v_mul_f32_e32 v139, 0x42800000, v111
	v_mul_f32_e32 v149, 0x42800000, v127
	ds_write_b128 v144, v[130:133] offset:32768
	v_mul_f32_e32 v131, 0x42800000, v67
	s_nop 0
	v_cvt_pk_fp8_f32 v130, v0, v131
	v_mul_f32_e32 v132, 0x42800000, v79
	v_mul_f32_e32 v133, 0x42800000, v75
	v_mul_f32_e32 v0, 0x42800000, v87
	v_cvt_pk_fp8_f32 v130, v132, v133 op_sel:[0,0,1]
	v_mul_f32_e32 v132, 0x42800000, v83
	v_cvt_pk_fp8_f32 v131, v0, v132
	v_mul_f32_e32 v133, 0x42800000, v95
	v_mul_f32_e32 v0, 0x42800000, v99
	v_cvt_pk_fp8_f32 v131, v133, v138 op_sel:[0,0,1]
	v_mul_f32_e32 v133, 0x42800000, v103
	v_cvt_pk_fp8_f32 v132, v0, v133
	v_mul_f32_e32 v138, 0x42800000, v107
	v_mul_f32_e32 v0, 0x42800000, v115
	v_cvt_pk_fp8_f32 v132, v138, v139 op_sel:[0,0,1]
	v_mul_f32_e32 v138, 0x42800000, v119
	v_cvt_pk_fp8_f32 v133, v0, v138
	v_mul_f32_e32 v139, 0x42800000, v123
	v_mul_f32_e32 v0, 0x42800000, v72
	v_mul_f32_e32 v138, 0x42800000, v92
	v_cvt_pk_fp8_f32 v133, v139, v149 op_sel:[0,0,1]
	v_mul_f32_e32 v139, 0x42800000, v112
	v_mul_f32_e32 v149, 0x42800000, v128
	s_cmp_lg_u32 s37, 0
	ds_write_b128 v144, v[130:133] offset:32896
	v_mul_f32_e32 v131, 0x42800000, v68
	s_nop 0
	v_cvt_pk_fp8_f32 v130, v0, v131
	v_mul_f32_e32 v132, 0x42800000, v80
	v_mul_f32_e32 v133, 0x42800000, v76
	v_mul_f32_e32 v0, 0x42800000, v88
	v_cvt_pk_fp8_f32 v130, v132, v133 op_sel:[0,0,1]
	v_mul_f32_e32 v132, 0x42800000, v84
	v_cvt_pk_fp8_f32 v131, v0, v132
	v_mul_f32_e32 v133, 0x42800000, v96
	v_mul_f32_e32 v0, 0x42800000, v100
	v_cvt_pk_fp8_f32 v131, v133, v138 op_sel:[0,0,1]
	v_mul_f32_e32 v133, 0x42800000, v104
	v_cvt_pk_fp8_f32 v132, v0, v133
	v_mul_f32_e32 v138, 0x42800000, v108
	v_mul_f32_e32 v0, 0x42800000, v116
	v_cvt_pk_fp8_f32 v132, v138, v139 op_sel:[0,0,1]
	v_mul_f32_e32 v138, 0x42800000, v120
	v_cvt_pk_fp8_f32 v133, v0, v138
	v_mul_f32_e32 v139, 0x42800000, v124
	v_mul_f32_e32 v0, 0x42800000, v73
	v_mul_f32_e32 v138, 0x42800000, v93
	v_cvt_pk_fp8_f32 v133, v139, v149 op_sel:[0,0,1]
	v_mul_f32_e32 v139, 0x42800000, v113
	v_mul_f32_e32 v149, 0x42800000, v129
	s_cselect_b64 s[18:19], -1, 0
	ds_write_b128 v144, v[130:133] offset:33024
	v_mul_f32_e32 v131, 0x42800000, v69
	s_nop 0
	v_cvt_pk_fp8_f32 v130, v0, v131
	v_mul_f32_e32 v132, 0x42800000, v81
	v_mul_f32_e32 v133, 0x42800000, v77
	v_mul_f32_e32 v0, 0x42800000, v89
	v_cvt_pk_fp8_f32 v130, v132, v133 op_sel:[0,0,1]
	v_mul_f32_e32 v132, 0x42800000, v85
	v_cvt_pk_fp8_f32 v131, v0, v132
	v_mul_f32_e32 v133, 0x42800000, v97
	v_mul_f32_e32 v0, 0x42800000, v101
	v_cvt_pk_fp8_f32 v131, v133, v138 op_sel:[0,0,1]
	v_mul_f32_e32 v133, 0x42800000, v105
	v_cvt_pk_fp8_f32 v132, v0, v133
	v_mul_f32_e32 v138, 0x42800000, v109
	v_mul_f32_e32 v0, 0x42800000, v117
	v_cvt_pk_fp8_f32 v132, v138, v139 op_sel:[0,0,1]
	v_mul_f32_e32 v138, 0x42800000, v121
	v_cvt_pk_fp8_f32 v133, v0, v138
	v_mul_f32_e32 v139, 0x42800000, v125
	v_add_u32_e32 v138, s12, v140
	s_cmp_eq_u32 s37, 0
	v_cvt_pk_fp8_f32 v133, v139, v149 op_sel:[0,0,1]
	ds_write_b128 v144, v[130:133] offset:33152
	s_waitcnt lgkmcnt(0)
	s_barrier
	ds_read_b128 v[130:133], v145 offset:32768
	s_cbranch_scc1 .LBB0_618
	v_cmp_lt_i32_e32 vcc, s47, v138
	v_lshlrev_b32_e32 v0, 1, v138
	v_and_b32_e32 v139, 0x7f, v138
	s_and_saveexec_b64 s[6:7], vcc
	s_xor_b64 s[6:7], exec, s[6:7]
	v_add_u32_e32 v0, 0x7ffff800, v0
	v_and_b32_e32 v0, 0x7fffff00, v0
	v_or3_b32 v138, v139, v0, s64
	s_andn2_saveexec_b64 s[6:7], s[6:7]
	v_and_or_b32 v138, v0, s65, v139
	s_or_b64 exec, exec, s[6:7]

.LBB0_655:
	s_waitcnt vmcnt(15)
	v_mul_f32_e32 v0, 0x42800000, v2
	s_waitcnt vmcnt(14)
	v_mul_f32_e32 v131, 0x42800000, v6
	v_cvt_pk_fp8_f32 v130, v0, v131
	s_waitcnt vmcnt(13)
	v_mul_f32_e32 v132, 0x42800000, v10
	s_waitcnt vmcnt(12)
	v_mul_f32_e32 v133, 0x42800000, v14
	s_waitcnt vmcnt(11)
	v_mul_f32_e32 v0, 0x42800000, v18
	v_cvt_pk_fp8_f32 v130, v132, v133 op_sel:[0,0,1]
	s_waitcnt vmcnt(10)
	v_mul_f32_e32 v132, 0x42800000, v22
	v_cvt_pk_fp8_f32 v131, v0, v132
	s_waitcnt vmcnt(9)
	v_mul_f32_e32 v133, 0x42800000, v26
	s_waitcnt vmcnt(8)
	v_mul_f32_e32 v138, 0x42800000, v30
	s_waitcnt vmcnt(7)
	v_mul_f32_e32 v0, 0x42800000, v34
	v_cvt_pk_fp8_f32 v131, v133, v138 op_sel:[0,0,1]
	s_waitcnt vmcnt(6)
	v_mul_f32_e32 v133, 0x42800000, v38
	v_cvt_pk_fp8_f32 v132, v0, v133
	s_waitcnt vmcnt(5)
	v_mul_f32_e32 v138, 0x42800000, v42
	s_waitcnt vmcnt(4)
	v_mul_f32_e32 v139, 0x42800000, v46
	s_waitcnt vmcnt(3)
	v_mul_f32_e32 v0, 0x42800000, v50
	v_cvt_pk_fp8_f32 v132, v138, v139 op_sel:[0,0,1]
	s_waitcnt vmcnt(2)
	v_mul_f32_e32 v138, 0x42800000, v54
	v_cvt_pk_fp8_f32 v133, v0, v138
	s_waitcnt vmcnt(1)
	v_mul_f32_e32 v139, 0x42800000, v58
	s_waitcnt vmcnt(0)
	v_mul_f32_e32 v149, 0x42800000, v62
	v_mul_f32_e32 v0, 0x42800000, v3
	v_cvt_pk_fp8_f32 v133, v139, v149 op_sel:[0,0,1]
	v_mul_f32_e32 v138, 0x42800000, v31
	v_mul_f32_e32 v139, 0x42800000, v47
	v_mul_f32_e32 v149, 0x42800000, v63
	ds_write_b128 v144, v[130:133]
	v_mul_f32_e32 v131, 0x42800000, v7
	s_nop 0
	v_cvt_pk_fp8_f32 v130, v0, v131
	v_mul_f32_e32 v132, 0x42800000, v11
	v_mul_f32_e32 v133, 0x42800000, v15
	v_mul_f32_e32 v0, 0x42800000, v19
	v_cvt_pk_fp8_f32 v130, v132, v133 op_sel:[0,0,1]
	v_mul_f32_e32 v132, 0x42800000, v23
	v_cvt_pk_fp8_f32 v131, v0, v132
	v_mul_f32_e32 v133, 0x42800000, v27
	v_mul_f32_e32 v0, 0x42800000, v35
	v_cvt_pk_fp8_f32 v131, v133, v138 op_sel:[0,0,1]
	v_mul_f32_e32 v133, 0x42800000, v39
	v_cvt_pk_fp8_f32 v132, v0, v133
	v_mul_f32_e32 v138, 0x42800000, v43
	v_mul_f32_e32 v0, 0x42800000, v51
	v_cvt_pk_fp8_f32 v132, v138, v139 op_sel:[0,0,1]
	v_mul_f32_e32 v138, 0x42800000, v55
	v_cvt_pk_fp8_f32 v133, v0, v138
	v_mul_f32_e32 v139, 0x42800000, v59
	v_mul_f32_e32 v0, 0x42800000, v4
	v_mul_f32_e32 v138, 0x42800000, v32
	v_cvt_pk_fp8_f32 v133, v139, v149 op_sel:[0,0,1]
	v_mul_f32_e32 v139, 0x42800000, v48
	v_mul_f32_e32 v149, 0x42800000, v64
	s_cmp_lg_u32 s36, 0
	ds_write_b128 v144, v[130:133] offset:128
	v_mul_f32_e32 v131, 0x42800000, v8
	s_nop 0
	v_cvt_pk_fp8_f32 v130, v0, v131
	v_mul_f32_e32 v132, 0x42800000, v12
	v_mul_f32_e32 v133, 0x42800000, v16
	v_mul_f32_e32 v0, 0x42800000, v20
	v_cvt_pk_fp8_f32 v130, v132, v133 op_sel:[0,0,1]
	v_mul_f32_e32 v132, 0x42800000, v24
	v_cvt_pk_fp8_f32 v131, v0, v132
	v_mul_f32_e32 v133, 0x42800000, v28
	v_mul_f32_e32 v0, 0x42800000, v36
	v_cvt_pk_fp8_f32 v131, v133, v138 op_sel:[0,0,1]
	v_mul_f32_e32 v133, 0x42800000, v40
	v_cvt_pk_fp8_f32 v132, v0, v133
	v_mul_f32_e32 v138, 0x42800000, v44
	v_mul_f32_e32 v0, 0x42800000, v52
	v_cvt_pk_fp8_f32 v132, v138, v139 op_sel:[0,0,1]
	v_mul_f32_e32 v138, 0x42800000, v56
	v_cvt_pk_fp8_f32 v133, v0, v138
	v_mul_f32_e32 v139, 0x42800000, v60
	v_mul_f32_e32 v0, 0x42800000, v5
	v_mul_f32_e32 v138, 0x42800000, v33
	v_cvt_pk_fp8_f32 v133, v139, v149 op_sel:[0,0,1]
	v_mul_f32_e32 v139, 0x42800000, v49
	v_mul_f32_e32 v149, 0x42800000, v65
	s_cselect_b64 s[20:21], -1, 0
	ds_write_b128 v144, v[130:133] offset:256
	v_mul_f32_e32 v131, 0x42800000, v9
	s_nop 0
	v_cvt_pk_fp8_f32 v130, v0, v131
	v_mul_f32_e32 v132, 0x42800000, v13
	v_mul_f32_e32 v133, 0x42800000, v17
	v_mul_f32_e32 v0, 0x42800000, v21
	v_cvt_pk_fp8_f32 v130, v132, v133 op_sel:[0,0,1]
	v_mul_f32_e32 v132, 0x42800000, v25
	v_cvt_pk_fp8_f32 v131, v0, v132
	v_mul_f32_e32 v133, 0x42800000, v29
	v_mul_f32_e32 v0, 0x42800000, v37
	v_cvt_pk_fp8_f32 v131, v133, v138 op_sel:[0,0,1]
	v_mul_f32_e32 v133, 0x42800000, v41
	v_cvt_pk_fp8_f32 v132, v0, v133
	v_mul_f32_e32 v138, 0x42800000, v45
	v_mul_f32_e32 v0, 0x42800000, v53
	v_cvt_pk_fp8_f32 v132, v138, v139 op_sel:[0,0,1]
	v_mul_f32_e32 v138, 0x42800000, v57
	v_cvt_pk_fp8_f32 v133, v0, v138
	v_mul_f32_e32 v139, 0x42800000, v61
	v_add_u32_e32 v138, s8, v140
	s_cmp_eq_u32 s36, 0
	v_cvt_pk_fp8_f32 v133, v139, v149 op_sel:[0,0,1]
	ds_write_b128 v144, v[130:133] offset:384
	s_waitcnt lgkmcnt(0)
	s_barrier
	ds_read_b128 v[130:133], v145
	s_cbranch_scc1 .LBB0_661
	v_cmp_lt_i32_e32 vcc, s47, v138
	v_lshlrev_b32_e32 v0, 1, v138
	v_and_b32_e32 v139, 0x7f, v138
	s_and_saveexec_b64 s[6:7], vcc
	s_xor_b64 s[6:7], exec, s[6:7]
	v_add_u32_e32 v0, 0x7ffff800, v0
	v_and_b32_e32 v0, 0x7fffff00, v0
	v_or3_b32 v138, v139, v0, s64
	s_andn2_saveexec_b64 s[6:7], s[6:7]
	v_and_or_b32 v138, v0, s65, v139
	s_or_b64 exec, exec, s[6:7]

.LBB0_687:
	v_mul_f32_e32 v0, 0x42800000, v70
	v_mul_f32_e32 v131, 0x42800000, v66
	s_nop 0
	v_cvt_pk_fp8_f32 v130, v0, v131
	v_mul_f32_e32 v132, 0x42800000, v78
	v_mul_f32_e32 v133, 0x42800000, v74
	v_mul_f32_e32 v0, 0x42800000, v86
	v_cvt_pk_fp8_f32 v130, v132, v133 op_sel:[0,0,1]
	v_mul_f32_e32 v132, 0x42800000, v82
	v_cvt_pk_fp8_f32 v131, v0, v132
	v_mul_f32_e32 v133, 0x42800000, v94
	v_mul_f32_e32 v138, 0x42800000, v90
	v_mul_f32_e32 v0, 0x42800000, v98
	v_cvt_pk_fp8_f32 v131, v133, v138 op_sel:[0,0,1]
	v_mul_f32_e32 v133, 0x42800000, v102
	v_cvt_pk_fp8_f32 v132, v0, v133
	v_mul_f32_e32 v138, 0x42800000, v106
	v_mul_f32_e32 v139, 0x42800000, v110
	v_mul_f32_e32 v0, 0x42800000, v114
	v_cvt_pk_fp8_f32 v132, v138, v139 op_sel:[0,0,1]
	v_mul_f32_e32 v138, 0x42800000, v118
	v_cvt_pk_fp8_f32 v133, v0, v138
	v_mul_f32_e32 v139, 0x42800000, v122
	v_mul_f32_e32 v149, 0x42800000, v126
	v_mul_f32_e32 v0, 0x42800000, v71
	v_cvt_pk_fp8_f32 v133, v139, v149 op_sel:[0,0,1]
	v_mul_f32_e32 v138, 0x42800000, v91
	v_mul_f32_e32 v139, 0x42800000, v111
	v_mul_f32_e32 v149, 0x42800000, v127
	ds_write_b128 v144, v[130:133] offset:32768
	v_mul_f32_e32 v131, 0x42800000, v67
	s_nop 0
	v_cvt_pk_fp8_f32 v130, v0, v131
	v_mul_f32_e32 v132, 0x42800000, v79
	v_mul_f32_e32 v133, 0x42800000, v75
	v_mul_f32_e32 v0, 0x42800000, v87
	v_cvt_pk_fp8_f32 v130, v132, v133 op_sel:[0,0,1]
	v_mul_f32_e32 v132, 0x42800000, v83
	v_cvt_pk_fp8_f32 v131, v0, v132
	v_mul_f32_e32 v133, 0x42800000, v95
	v_mul_f32_e32 v0, 0x42800000, v99
	v_cvt_pk_fp8_f32 v131, v133, v138 op_sel:[0,0,1]
	v_mul_f32_e32 v133, 0x42800000, v103
	v_cvt_pk_fp8_f32 v132, v0, v133
	v_mul_f32_e32 v138, 0x42800000, v107
	v_mul_f32_e32 v0, 0x42800000, v115
	v_cvt_pk_fp8_f32 v132, v138, v139 op_sel:[0,0,1]
	v_mul_f32_e32 v138, 0x42800000, v119
	v_cvt_pk_fp8_f32 v133, v0, v138
	v_mul_f32_e32 v139, 0x42800000, v123
	v_mul_f32_e32 v0, 0x42800000, v72
	v_mul_f32_e32 v138, 0x42800000, v92
	v_cvt_pk_fp8_f32 v133, v139, v149 op_sel:[0,0,1]
	v_mul_f32_e32 v139, 0x42800000, v112
	v_mul_f32_e32 v149, 0x42800000, v128
	s_cmp_lg_u32 s40, 0
	ds_write_b128 v144, v[130:133] offset:32896
	v_mul_f32_e32 v131, 0x42800000, v68
	s_nop 0
	v_cvt_pk_fp8_f32 v130, v0, v131
	v_mul_f32_e32 v132, 0x42800000, v80
	v_mul_f32_e32 v133, 0x42800000, v76
	v_mul_f32_e32 v0, 0x42800000, v88
	v_cvt_pk_fp8_f32 v130, v132, v133 op_sel:[0,0,1]
	v_mul_f32_e32 v132, 0x42800000, v84
	v_cvt_pk_fp8_f32 v131, v0, v132
	v_mul_f32_e32 v133, 0x42800000, v96
	v_mul_f32_e32 v0, 0x42800000, v100
	v_cvt_pk_fp8_f32 v131, v133, v138 op_sel:[0,0,1]
	v_mul_f32_e32 v133, 0x42800000, v104
	v_cvt_pk_fp8_f32 v132, v0, v133
	v_mul_f32_e32 v138, 0x42800000, v108
	v_mul_f32_e32 v0, 0x42800000, v116
	v_cvt_pk_fp8_f32 v132, v138, v139 op_sel:[0,0,1]
	v_mul_f32_e32 v138, 0x42800000, v120
	v_cvt_pk_fp8_f32 v133, v0, v138
	v_mul_f32_e32 v139, 0x42800000, v124
	v_mul_f32_e32 v0, 0x42800000, v73
	v_mul_f32_e32 v138, 0x42800000, v93
	v_cvt_pk_fp8_f32 v133, v139, v149 op_sel:[0,0,1]
	v_mul_f32_e32 v139, 0x42800000, v113
	v_mul_f32_e32 v149, 0x42800000, v129
	s_cselect_b64 s[18:19], -1, 0
	ds_write_b128 v144, v[130:133] offset:33024
	v_mul_f32_e32 v131, 0x42800000, v69
	s_nop 0
	v_cvt_pk_fp8_f32 v130, v0, v131
	v_mul_f32_e32 v132, 0x42800000, v81
	v_mul_f32_e32 v133, 0x42800000, v77
	v_mul_f32_e32 v0, 0x42800000, v89
	v_cvt_pk_fp8_f32 v130, v132, v133 op_sel:[0,0,1]
	v_mul_f32_e32 v132, 0x42800000, v85
	v_cvt_pk_fp8_f32 v131, v0, v132
	v_mul_f32_e32 v133, 0x42800000, v97
	v_mul_f32_e32 v0, 0x42800000, v101
	v_cvt_pk_fp8_f32 v131, v133, v138 op_sel:[0,0,1]
	v_mul_f32_e32 v133, 0x42800000, v105
	v_cvt_pk_fp8_f32 v132, v0, v133
	v_mul_f32_e32 v138, 0x42800000, v109
	v_mul_f32_e32 v0, 0x42800000, v117
	v_cvt_pk_fp8_f32 v132, v138, v139 op_sel:[0,0,1]
	v_mul_f32_e32 v138, 0x42800000, v121
	v_cvt_pk_fp8_f32 v133, v0, v138
	v_mul_f32_e32 v139, 0x42800000, v125
	v_add_u32_e32 v138, s12, v140
	s_cmp_eq_u32 s40, 0
	v_cvt_pk_fp8_f32 v133, v139, v149 op_sel:[0,0,1]
	ds_write_b128 v144, v[130:133] offset:33152
	s_waitcnt lgkmcnt(0)
	s_barrier
	ds_read_b128 v[130:133], v145 offset:32768
	s_cbranch_scc1 .LBB0_693
	v_cmp_lt_i32_e32 vcc, s47, v138
	v_lshlrev_b32_e32 v0, 1, v138
	v_and_b32_e32 v139, 0x7f, v138
	s_and_saveexec_b64 s[6:7], vcc
	s_xor_b64 s[6:7], exec, s[6:7]
	v_add_u32_e32 v0, 0x7ffff800, v0
	v_and_b32_e32 v0, 0x7fffff00, v0
	v_or3_b32 v138, v139, v0, s64
	s_andn2_saveexec_b64 s[6:7], s[6:7]
	v_and_or_b32 v138, v0, s65, v139
	s_or_b64 exec, exec, s[6:7]

.Lcvm_a_ready:
	v_mul_f32_e32 v0, 0x42800000, v2
	v_mul_f32_e32 v131, 0x42800000, v6
	v_cvt_pk_fp8_f32 v130, v0, v131
	v_mul_f32_e32 v132, 0x42800000, v10
	v_mul_f32_e32 v133, 0x42800000, v14
	v_mul_f32_e32 v0, 0x42800000, v18
	v_cvt_pk_fp8_f32 v130, v132, v133 op_sel:[0,0,1]
	v_mul_f32_e32 v132, 0x42800000, v22
	v_cvt_pk_fp8_f32 v131, v0, v132
	v_mul_f32_e32 v133, 0x42800000, v26
	v_mul_f32_e32 v138, 0x42800000, v30
	v_mul_f32_e32 v0, 0x42800000, v34
	v_cvt_pk_fp8_f32 v131, v133, v138 op_sel:[0,0,1]
	v_mul_f32_e32 v133, 0x42800000, v38
	v_cvt_pk_fp8_f32 v132, v0, v133
	v_mul_f32_e32 v138, 0x42800000, v42
	v_mul_f32_e32 v139, 0x42800000, v46
	v_mul_f32_e32 v0, 0x42800000, v50
	v_cvt_pk_fp8_f32 v132, v138, v139 op_sel:[0,0,1]
	v_mul_f32_e32 v138, 0x42800000, v54
	v_cvt_pk_fp8_f32 v133, v0, v138
	v_mul_f32_e32 v139, 0x42800000, v58
	v_mul_f32_e32 v149, 0x42800000, v62
	v_mul_f32_e32 v0, 0x42800000, v3
	v_cvt_pk_fp8_f32 v133, v139, v149 op_sel:[0,0,1]
	v_mul_f32_e32 v138, 0x42800000, v31
	v_mul_f32_e32 v139, 0x42800000, v47
	v_mul_f32_e32 v149, 0x42800000, v63
	ds_write_b128 v144, v[130:133]
	v_mul_f32_e32 v131, 0x42800000, v7
	s_nop 0
	v_cvt_pk_fp8_f32 v130, v0, v131
	v_mul_f32_e32 v132, 0x42800000, v11
	v_mul_f32_e32 v133, 0x42800000, v15
	v_mul_f32_e32 v0, 0x42800000, v19
	v_cvt_pk_fp8_f32 v130, v132, v133 op_sel:[0,0,1]
	v_mul_f32_e32 v132, 0x42800000, v23
	v_cvt_pk_fp8_f32 v131, v0, v132
	v_mul_f32_e32 v133, 0x42800000, v27
	v_mul_f32_e32 v0, 0x42800000, v35
	v_cvt_pk_fp8_f32 v131, v133, v138 op_sel:[0,0,1]
	v_mul_f32_e32 v133, 0x42800000, v39
	v_cvt_pk_fp8_f32 v132, v0, v133
	v_mul_f32_e32 v138, 0x42800000, v43
	v_mul_f32_e32 v0, 0x42800000, v51
	v_cvt_pk_fp8_f32 v132, v138, v139 op_sel:[0,0,1]
	v_mul_f32_e32 v138, 0x42800000, v55
	v_cvt_pk_fp8_f32 v133, v0, v138
	v_mul_f32_e32 v139, 0x42800000, v59
	v_mul_f32_e32 v0, 0x42800000, v4
	v_mul_f32_e32 v138, 0x42800000, v32
	v_cvt_pk_fp8_f32 v133, v139, v149 op_sel:[0,0,1]
	v_mul_f32_e32 v139, 0x42800000, v48
	v_mul_f32_e32 v149, 0x42800000, v64
	s_cmp_lg_u32 s36, 0
	ds_write_b128 v144, v[130:133] offset:128
	v_mul_f32_e32 v131, 0x42800000, v8
	s_nop 0
	v_cvt_pk_fp8_f32 v130, v0, v131
	v_mul_f32_e32 v132, 0x42800000, v12
	v_mul_f32_e32 v133, 0x42800000, v16
	v_mul_f32_e32 v0, 0x42800000, v20
	v_cvt_pk_fp8_f32 v130, v132, v133 op_sel:[0,0,1]
	v_mul_f32_e32 v132, 0x42800000, v24
	v_cvt_pk_fp8_f32 v131, v0, v132
	v_mul_f32_e32 v133, 0x42800000, v28
	v_mul_f32_e32 v0, 0x42800000, v36
	v_cvt_pk_fp8_f32 v131, v133, v138 op_sel:[0,0,1]
	v_mul_f32_e32 v133, 0x42800000, v40
	v_cvt_pk_fp8_f32 v132, v0, v133
	v_mul_f32_e32 v138, 0x42800000, v44
	v_mul_f32_e32 v0, 0x42800000, v52
	v_cvt_pk_fp8_f32 v132, v138, v139 op_sel:[0,0,1]
	v_mul_f32_e32 v138, 0x42800000, v56
	v_cvt_pk_fp8_f32 v133, v0, v138
	v_mul_f32_e32 v139, 0x42800000, v60
	v_mul_f32_e32 v0, 0x42800000, v5
	v_mul_f32_e32 v138, 0x42800000, v33
	v_cvt_pk_fp8_f32 v133, v139, v149 op_sel:[0,0,1]
	v_mul_f32_e32 v139, 0x42800000, v49
	v_mul_f32_e32 v149, 0x42800000, v65
	s_cselect_b64 s[34:35], -1, 0
	ds_write_b128 v144, v[130:133] offset:256
	v_mul_f32_e32 v131, 0x42800000, v9
	s_nop 0
	v_cvt_pk_fp8_f32 v130, v0, v131
	v_mul_f32_e32 v132, 0x42800000, v13
	v_mul_f32_e32 v133, 0x42800000, v17
	v_mul_f32_e32 v0, 0x42800000, v21
	v_cvt_pk_fp8_f32 v130, v132, v133 op_sel:[0,0,1]
	v_mul_f32_e32 v132, 0x42800000, v25
	v_cvt_pk_fp8_f32 v131, v0, v132
	v_mul_f32_e32 v133, 0x42800000, v29
	v_mul_f32_e32 v0, 0x42800000, v37
	v_cvt_pk_fp8_f32 v131, v133, v138 op_sel:[0,0,1]
	v_mul_f32_e32 v133, 0x42800000, v41
	v_cvt_pk_fp8_f32 v132, v0, v133
	v_mul_f32_e32 v138, 0x42800000, v45
	v_mul_f32_e32 v0, 0x42800000, v53
	v_cvt_pk_fp8_f32 v132, v138, v139 op_sel:[0,0,1]
	v_mul_f32_e32 v138, 0x42800000, v57
	v_cvt_pk_fp8_f32 v133, v0, v138
	v_mul_f32_e32 v139, 0x42800000, v61
	v_add_u32_e32 v138, s10, v140
	s_cmp_eq_u32 s36, 0
	v_cvt_pk_fp8_f32 v133, v139, v149 op_sel:[0,0,1]
	ds_write_b128 v144, v[130:133] offset:384
	s_waitcnt lgkmcnt(0)
	s_barrier
	ds_read_b128 v[130:133], v145
	s_cbranch_scc1 .LBB0_1003
	v_cmp_lt_i32_e32 vcc, s47, v138
	v_lshlrev_b32_e32 v0, 1, v138
	v_and_b32_e32 v139, 0x7f, v138
	s_and_saveexec_b64 s[8:9], vcc
	s_xor_b64 s[8:9], exec, s[8:9]
	v_add_u32_e32 v0, 0x7ffff800, v0
	v_and_b32_e32 v0, 0x7fffff00, v0
	v_or3_b32 v138, v139, v0, s64
	s_andn2_saveexec_b64 s[8:9], s[8:9]
	v_and_or_b32 v138, v0, s65, v139
	s_or_b64 exec, exec, s[8:9]

.Lcvm_b_ready:
	v_mul_f32_e32 v0, 0x42800000, v70
	v_mul_f32_e32 v131, 0x42800000, v66
	s_nop 0
	v_cvt_pk_fp8_f32 v130, v0, v131
	v_mul_f32_e32 v132, 0x42800000, v78
	v_mul_f32_e32 v133, 0x42800000, v74
	v_mul_f32_e32 v0, 0x42800000, v86
	v_cvt_pk_fp8_f32 v130, v132, v133 op_sel:[0,0,1]
	v_mul_f32_e32 v132, 0x42800000, v82
	v_cvt_pk_fp8_f32 v131, v0, v132
	v_mul_f32_e32 v133, 0x42800000, v94
	v_mul_f32_e32 v138, 0x42800000, v90
	v_mul_f32_e32 v0, 0x42800000, v98
	v_cvt_pk_fp8_f32 v131, v133, v138 op_sel:[0,0,1]
	v_mul_f32_e32 v133, 0x42800000, v102
	v_cvt_pk_fp8_f32 v132, v0, v133
	v_mul_f32_e32 v138, 0x42800000, v106
	v_mul_f32_e32 v139, 0x42800000, v110
	v_mul_f32_e32 v0, 0x42800000, v114
	v_cvt_pk_fp8_f32 v132, v138, v139 op_sel:[0,0,1]
	v_mul_f32_e32 v138, 0x42800000, v118
	v_cvt_pk_fp8_f32 v133, v0, v138
	v_mul_f32_e32 v139, 0x42800000, v122
	v_mul_f32_e32 v149, 0x42800000, v126
	v_mul_f32_e32 v0, 0x42800000, v71
	v_cvt_pk_fp8_f32 v133, v139, v149 op_sel:[0,0,1]
	v_mul_f32_e32 v138, 0x42800000, v91
	v_mul_f32_e32 v139, 0x42800000, v111
	v_mul_f32_e32 v149, 0x42800000, v127
	ds_write_b128 v144, v[130:133] offset:32768
	v_mul_f32_e32 v131, 0x42800000, v67
	s_nop 0
	v_cvt_pk_fp8_f32 v130, v0, v131
	v_mul_f32_e32 v132, 0x42800000, v79
	v_mul_f32_e32 v133, 0x42800000, v75
	v_mul_f32_e32 v0, 0x42800000, v87
	v_cvt_pk_fp8_f32 v130, v132, v133 op_sel:[0,0,1]
	v_mul_f32_e32 v132, 0x42800000, v83
	v_cvt_pk_fp8_f32 v131, v0, v132
	v_mul_f32_e32 v133, 0x42800000, v95
	v_mul_f32_e32 v0, 0x42800000, v99
	v_cvt_pk_fp8_f32 v131, v133, v138 op_sel:[0,0,1]
	v_mul_f32_e32 v133, 0x42800000, v103
	v_cvt_pk_fp8_f32 v132, v0, v133
	v_mul_f32_e32 v138, 0x42800000, v107
	v_mul_f32_e32 v0, 0x42800000, v115
	v_cvt_pk_fp8_f32 v132, v138, v139 op_sel:[0,0,1]
	v_mul_f32_e32 v138, 0x42800000, v119
	v_cvt_pk_fp8_f32 v133, v0, v138
	v_mul_f32_e32 v139, 0x42800000, v123
	v_mul_f32_e32 v0, 0x42800000, v72
	v_mul_f32_e32 v138, 0x42800000, v92
	v_cvt_pk_fp8_f32 v133, v139, v149 op_sel:[0,0,1]
	v_mul_f32_e32 v139, 0x42800000, v112
	v_mul_f32_e32 v149, 0x42800000, v128
	s_cmp_lg_u32 s45, 0
	ds_write_b128 v144, v[130:133] offset:32896
	v_mul_f32_e32 v131, 0x42800000, v68
	s_nop 0
	v_cvt_pk_fp8_f32 v130, v0, v131
	v_mul_f32_e32 v132, 0x42800000, v80
	v_mul_f32_e32 v133, 0x42800000, v76
	v_mul_f32_e32 v0, 0x42800000, v88
	v_cvt_pk_fp8_f32 v130, v132, v133 op_sel:[0,0,1]
	v_mul_f32_e32 v132, 0x42800000, v84
	v_cvt_pk_fp8_f32 v131, v0, v132
	v_mul_f32_e32 v133, 0x42800000, v96
	v_mul_f32_e32 v0, 0x42800000, v100
	v_cvt_pk_fp8_f32 v131, v133, v138 op_sel:[0,0,1]
	v_mul_f32_e32 v133, 0x42800000, v104
	v_cvt_pk_fp8_f32 v132, v0, v133
	v_mul_f32_e32 v138, 0x42800000, v108
	v_mul_f32_e32 v0, 0x42800000, v116
	v_cvt_pk_fp8_f32 v132, v138, v139 op_sel:[0,0,1]
	v_mul_f32_e32 v138, 0x42800000, v120
	v_cvt_pk_fp8_f32 v133, v0, v138
	v_mul_f32_e32 v139, 0x42800000, v124
	v_mul_f32_e32 v0, 0x42800000, v73
	v_mul_f32_e32 v138, 0x42800000, v93
	v_cvt_pk_fp8_f32 v133, v139, v149 op_sel:[0,0,1]
	v_mul_f32_e32 v139, 0x42800000, v113
	v_mul_f32_e32 v149, 0x42800000, v129
	s_cselect_b64 s[34:35], -1, 0
	ds_write_b128 v144, v[130:133] offset:33024
	v_mul_f32_e32 v131, 0x42800000, v69
	s_nop 0
	v_cvt_pk_fp8_f32 v130, v0, v131
	v_mul_f32_e32 v132, 0x42800000, v81
	v_mul_f32_e32 v133, 0x42800000, v77
	v_mul_f32_e32 v0, 0x42800000, v89
	v_cvt_pk_fp8_f32 v130, v132, v133 op_sel:[0,0,1]
	v_mul_f32_e32 v132, 0x42800000, v85
	v_cvt_pk_fp8_f32 v131, v0, v132
	v_mul_f32_e32 v133, 0x42800000, v97
	v_mul_f32_e32 v0, 0x42800000, v101
	v_cvt_pk_fp8_f32 v131, v133, v138 op_sel:[0,0,1]
	v_mul_f32_e32 v133, 0x42800000, v105
	v_cvt_pk_fp8_f32 v132, v0, v133
	v_mul_f32_e32 v138, 0x42800000, v109
	v_mul_f32_e32 v0, 0x42800000, v117
	v_cvt_pk_fp8_f32 v132, v138, v139 op_sel:[0,0,1]
	v_mul_f32_e32 v138, 0x42800000, v121
	v_cvt_pk_fp8_f32 v133, v0, v138
	v_mul_f32_e32 v139, 0x42800000, v125
	v_add_u32_e32 v138, s24, v140
	s_cmp_eq_u32 s45, 0
	v_cvt_pk_fp8_f32 v133, v139, v149 op_sel:[0,0,1]
	ds_write_b128 v144, v[130:133] offset:33152
	s_waitcnt lgkmcnt(0)
	s_barrier
	ds_read_b128 v[130:133], v145 offset:32768
	s_cbranch_scc1 .LBB0_1035
	v_cmp_lt_i32_e32 vcc, s47, v138
	v_lshlrev_b32_e32 v0, 1, v138
	v_and_b32_e32 v139, 0x7f, v138
	s_and_saveexec_b64 s[8:9], vcc
	s_xor_b64 s[8:9], exec, s[8:9]
	v_add_u32_e32 v0, 0x7ffff800, v0
	v_and_b32_e32 v0, 0x7fffff00, v0
	v_or3_b32 v138, v139, v0, s64
	s_andn2_saveexec_b64 s[8:9], s[8:9]
	v_and_or_b32 v138, v0, s65, v139
	s_or_b64 exec, exec, s[8:9]

.LBB0_1423:
	s_waitcnt vmcnt(15)
	v_mul_f32_e32 v0, 0x42800000, v2
	s_waitcnt vmcnt(14)
	v_mul_f32_e32 v131, 0x42800000, v6
	v_cvt_pk_fp8_f32 v130, v0, v131
	s_waitcnt vmcnt(13)
	v_mul_f32_e32 v132, 0x42800000, v10
	s_waitcnt vmcnt(12)
	v_mul_f32_e32 v133, 0x42800000, v14
	s_waitcnt vmcnt(11)
	v_mul_f32_e32 v0, 0x42800000, v18
	v_cvt_pk_fp8_f32 v130, v132, v133 op_sel:[0,0,1]
	s_waitcnt vmcnt(10)
	v_mul_f32_e32 v132, 0x42800000, v22
	v_cvt_pk_fp8_f32 v131, v0, v132
	s_waitcnt vmcnt(9)
	v_mul_f32_e32 v133, 0x42800000, v26
	s_waitcnt vmcnt(8)
	v_mul_f32_e32 v138, 0x42800000, v30
	s_waitcnt vmcnt(7)
	v_mul_f32_e32 v0, 0x42800000, v34
	v_cvt_pk_fp8_f32 v131, v133, v138 op_sel:[0,0,1]
	s_waitcnt vmcnt(6)
	v_mul_f32_e32 v133, 0x42800000, v38
	v_cvt_pk_fp8_f32 v132, v0, v133
	s_waitcnt vmcnt(5)
	v_mul_f32_e32 v138, 0x42800000, v42
	s_waitcnt vmcnt(4)
	v_mul_f32_e32 v139, 0x42800000, v46
	s_waitcnt vmcnt(3)
	v_mul_f32_e32 v0, 0x42800000, v50
	v_cvt_pk_fp8_f32 v132, v138, v139 op_sel:[0,0,1]
	s_waitcnt vmcnt(2)
	v_mul_f32_e32 v138, 0x42800000, v54
	v_cvt_pk_fp8_f32 v133, v0, v138
	s_waitcnt vmcnt(1)
	v_mul_f32_e32 v139, 0x42800000, v58
	s_waitcnt vmcnt(0)
	v_mul_f32_e32 v149, 0x42800000, v62
	v_mul_f32_e32 v0, 0x42800000, v3
	v_cvt_pk_fp8_f32 v133, v139, v149 op_sel:[0,0,1]
	v_mul_f32_e32 v138, 0x42800000, v31
	v_mul_f32_e32 v139, 0x42800000, v47
	v_mul_f32_e32 v149, 0x42800000, v63
	ds_write_b128 v144, v[130:133]
	v_mul_f32_e32 v131, 0x42800000, v7
	s_nop 0
	v_cvt_pk_fp8_f32 v130, v0, v131
	v_mul_f32_e32 v132, 0x42800000, v11
	v_mul_f32_e32 v133, 0x42800000, v15
	v_mul_f32_e32 v0, 0x42800000, v19
	v_cvt_pk_fp8_f32 v130, v132, v133 op_sel:[0,0,1]
	v_mul_f32_e32 v132, 0x42800000, v23
	v_cvt_pk_fp8_f32 v131, v0, v132
	v_mul_f32_e32 v133, 0x42800000, v27
	v_mul_f32_e32 v0, 0x42800000, v35
	v_cvt_pk_fp8_f32 v131, v133, v138 op_sel:[0,0,1]
	v_mul_f32_e32 v133, 0x42800000, v39
	v_cvt_pk_fp8_f32 v132, v0, v133
	v_mul_f32_e32 v138, 0x42800000, v43
	v_mul_f32_e32 v0, 0x42800000, v51
	v_cvt_pk_fp8_f32 v132, v138, v139 op_sel:[0,0,1]
	v_mul_f32_e32 v138, 0x42800000, v55
	v_cvt_pk_fp8_f32 v133, v0, v138
	v_mul_f32_e32 v139, 0x42800000, v59
	v_mul_f32_e32 v0, 0x42800000, v4
	v_mul_f32_e32 v138, 0x42800000, v32
	v_cvt_pk_fp8_f32 v133, v139, v149 op_sel:[0,0,1]
	v_mul_f32_e32 v139, 0x42800000, v48
	v_mul_f32_e32 v149, 0x42800000, v64
	s_cmp_lg_u32 s34, 0
	ds_write_b128 v144, v[130:133] offset:128
	v_mul_f32_e32 v131, 0x42800000, v8
	s_nop 0
	v_cvt_pk_fp8_f32 v130, v0, v131
	v_mul_f32_e32 v132, 0x42800000, v12
	v_mul_f32_e32 v133, 0x42800000, v16
	v_mul_f32_e32 v0, 0x42800000, v20
	v_cvt_pk_fp8_f32 v130, v132, v133 op_sel:[0,0,1]
	v_mul_f32_e32 v132, 0x42800000, v24
	v_cvt_pk_fp8_f32 v131, v0, v132
	v_mul_f32_e32 v133, 0x42800000, v28
	v_mul_f32_e32 v0, 0x42800000, v36
	v_cvt_pk_fp8_f32 v131, v133, v138 op_sel:[0,0,1]
	v_mul_f32_e32 v133, 0x42800000, v40
	v_cvt_pk_fp8_f32 v132, v0, v133
	v_mul_f32_e32 v138, 0x42800000, v44
	v_mul_f32_e32 v0, 0x42800000, v52
	v_cvt_pk_fp8_f32 v132, v138, v139 op_sel:[0,0,1]
	v_mul_f32_e32 v138, 0x42800000, v56
	v_cvt_pk_fp8_f32 v133, v0, v138
	v_mul_f32_e32 v139, 0x42800000, v60
	v_mul_f32_e32 v0, 0x42800000, v5
	v_mul_f32_e32 v138, 0x42800000, v33
	v_cvt_pk_fp8_f32 v133, v139, v149 op_sel:[0,0,1]
	v_mul_f32_e32 v139, 0x42800000, v49
	v_mul_f32_e32 v149, 0x42800000, v65
	s_cselect_b64 s[20:21], -1, 0
	ds_write_b128 v144, v[130:133] offset:256
	v_mul_f32_e32 v131, 0x42800000, v9
	s_nop 0
	v_cvt_pk_fp8_f32 v130, v0, v131
	v_mul_f32_e32 v132, 0x42800000, v13
	v_mul_f32_e32 v133, 0x42800000, v17
	v_mul_f32_e32 v0, 0x42800000, v21
	v_cvt_pk_fp8_f32 v130, v132, v133 op_sel:[0,0,1]
	v_mul_f32_e32 v132, 0x42800000, v25
	v_cvt_pk_fp8_f32 v131, v0, v132
	v_mul_f32_e32 v133, 0x42800000, v29
	v_mul_f32_e32 v0, 0x42800000, v37
	v_cvt_pk_fp8_f32 v131, v133, v138 op_sel:[0,0,1]
	v_mul_f32_e32 v133, 0x42800000, v41
	v_cvt_pk_fp8_f32 v132, v0, v133
	v_mul_f32_e32 v138, 0x42800000, v45
	v_mul_f32_e32 v0, 0x42800000, v53
	v_cvt_pk_fp8_f32 v132, v138, v139 op_sel:[0,0,1]
	v_mul_f32_e32 v138, 0x42800000, v57
	v_cvt_pk_fp8_f32 v133, v0, v138
	v_mul_f32_e32 v139, 0x42800000, v61
	v_add_u32_e32 v138, s8, v140
	s_cmp_eq_u32 s34, 0
	v_cvt_pk_fp8_f32 v133, v139, v149 op_sel:[0,0,1]
	ds_write_b128 v144, v[130:133] offset:384
	s_waitcnt lgkmcnt(0)
	s_barrier
	ds_read_b128 v[130:133], v145
	s_cbranch_scc1 .LBB0_1429
	v_cmp_lt_i32_e32 vcc, s47, v138
	v_lshlrev_b32_e32 v0, 1, v138
	v_and_b32_e32 v139, 0x7f, v138
	s_and_saveexec_b64 s[6:7], vcc
	s_xor_b64 s[6:7], exec, s[6:7]
	v_add_u32_e32 v0, 0x7ffff800, v0
	v_and_b32_e32 v0, 0x7fffff00, v0
	v_or3_b32 v138, v139, v0, s64
	s_andn2_saveexec_b64 s[6:7], s[6:7]
	v_and_or_b32 v138, v0, s65, v139
	s_or_b64 exec, exec, s[6:7]

.LBB0_1547:
	v_lshlrev_b32_e32 v157, 16, v137
	v_lshlrev_b32_e32 v156, 16, v136
	v_and_b32_e32 v137, 0xffff0000, v137
	v_and_b32_e32 v136, 0xffff0000, v136
	v_pk_mul_f32 v[172:173], v[136:137], v[136:137]
	v_lshlrev_b32_e32 v154, 16, v134
	v_pk_fma_f32 v[172:173], v[156:157], v[156:157], v[172:173]
	v_and_b32_e32 v155, 0xffff0000, v134
	v_lshlrev_b32_e32 v134, 16, v135
	v_lshlrev_b32_e32 v158, 16, v126
	v_pk_add_f32 v[172:173], v[172:173], v[172:173] op_sel_hi:[0,1]
	v_and_b32_e32 v135, 0xffff0000, v135
	v_and_b32_e32 v159, 0xffff0000, v126
	v_lshlrev_b32_e32 v126, 16, v127
	v_mul_f32_e32 v168, v154, v154
	v_mul_f32_e32 v170, v134, v134
	v_mul_f32_e32 v172, v158, v158
	v_and_b32_e32 v127, 0xffff0000, v127
	v_pk_fma_f32 v[168:169], v[154:155], v[154:155], v[168:169] op_sel_hi:[1,1,0]
	v_pk_fma_f32 v[170:171], v[134:135], v[134:135], v[170:171] op_sel_hi:[1,1,0]
	v_pk_fma_f32 v[174:175], v[158:159], v[158:159], v[172:173] op_sel_hi:[1,1,0]
	v_mul_f32_e32 v172, v126, v126
	v_lshlrev_b32_e32 v160, 16, v128
	v_and_b32_e32 v161, 0xffff0000, v128
	v_lshlrev_b32_e32 v128, 16, v129
	v_and_b32_e32 v129, 0xffff0000, v129
	v_pk_fma_f32 v[176:177], v[126:127], v[126:127], v[172:173] op_sel_hi:[1,1,0]
	v_pk_add_f32 v[168:169], v[168:169], v[170:171]
	v_mul_f32_e32 v172, v161, v161
	v_mul_f32_e32 v174, v128, v128
	v_mul_f32_e32 v176, v129, v129
	v_mul_f32_e32 v178, v160, v160
	v_mov_b32_e32 v179, v169
	v_pk_add_f32 v[168:169], v[178:179], v[172:173]
	v_pk_add_f32 v[170:171], v[174:175], v[176:177]
	v_lshlrev_b32_e32 v162, 16, v130
	v_pk_add_f32 v[168:169], v[168:169], v[170:171]
	v_and_b32_e32 v163, 0xffff0000, v130
	v_add_f32_e32 v168, v168, v169
	v_lshlrev_b32_e32 v130, 16, v131
	v_and_b32_e32 v131, 0xffff0000, v131
	v_add_f32_dpp v168, v168, v168 quad_perm:[1,0,3,2] row_mask:0xf bank_mask:0xf bound_ctrl:1
	v_lshlrev_b32_e32 v165, 16, v133
	v_lshlrev_b32_e32 v164, 16, v132
	v_add_f32_dpp v168, v168, v168 quad_perm:[2,3,0,1] row_mask:0xf bank_mask:0xf bound_ctrl:1
	v_and_b32_e32 v133, 0xffff0000, v133
	v_and_b32_e32 v132, 0xffff0000, v132
	v_add_f32_dpp v168, v168, v168 row_half_mirror row_mask:0xf bank_mask:0xf bound_ctrl:1
	v_lshlrev_b32_e32 v166, 16, v122
	v_and_b32_e32 v167, 0xffff0000, v122
	v_add_f32_dpp v170, v168, v168 row_mirror row_mask:0xf bank_mask:0xf bound_ctrl:1
	v_mbcnt_lo_u32_b32 v168, -1, 0
	v_mbcnt_hi_u32_b32 v168, -1, v168
	v_lshlrev_b32_e32 v122, 16, v123
	v_lshlrev_b32_e32 v168, 2, v168
	v_xor_b32_e32 v168, 64, v168
	ds_bpermute_b32 v171, v168, v170
	v_pk_mul_f32 v[178:179], v[132:133], v[132:133]
	v_and_b32_e32 v123, 0xffff0000, v123
	v_pk_fma_f32 v[178:179], v[164:165], v[164:165], v[178:179]
	v_lshlrev_b32_e32 v168, 16, v124
	s_waitcnt lgkmcnt(0)
	v_add_f32_e32 v171, v170, v171
	v_mov_b32_e32 v173, v171
	v_mul_f32_e32 v170, v162, v162
	s_nop 1
	v_permlane32_swap_b32 v173, v171
	v_and_b32_e32 v169, 0xffff0000, v124
	v_pk_fma_f32 v[174:175], v[162:163], v[162:163], v[170:171] op_sel_hi:[1,1,0]
	v_mul_f32_e32 v170, v130, v130
	v_pk_fma_f32 v[176:177], v[130:131], v[130:131], v[170:171] op_sel_hi:[1,1,0]
	v_mul_f32_e32 v170, v166, v166
	v_pk_fma_f32 v[180:181], v[166:167], v[166:167], v[170:171] op_sel_hi:[1,1,0]
	v_mul_f32_e32 v170, v122, v122
	v_lshlrev_b32_e32 v124, 16, v125
	v_and_b32_e32 v125, 0xffff0000, v125
	v_pk_add_f32 v[178:179], v[178:179], v[178:179] op_sel_hi:[0,1]
	v_pk_fma_f32 v[182:183], v[122:123], v[122:123], v[170:171] op_sel_hi:[1,1,0]
	v_pk_add_f32 v[174:175], v[174:175], v[176:177]
	v_mul_f32_e32 v178, v169, v169
	v_mul_f32_e32 v180, v124, v124
	v_mul_f32_e32 v182, v125, v125
	v_mul_f32_e32 v184, v168, v168
	v_mov_b32_e32 v185, v175
	v_pk_add_f32 v[174:175], v[184:185], v[178:179]
	v_pk_add_f32 v[176:177], v[180:181], v[182:183]
	v_mbcnt_lo_u32_b32 v172, -1, 0
	v_mbcnt_hi_u32_b32 v172, -1, v172
	s_mov_b32 s12, 0x3a800000
	v_pk_add_f32 v[174:175], v[174:175], v[176:177]
	v_lshlrev_b32_e32 v172, 2, v172
	v_add_f32_e32 v170, v174, v175
	v_xor_b32_e32 v172, 64, v172
	s_ashr_i32 s17, s16, 31
	v_add_f32_dpp v170, v170, v170 quad_perm:[1,0,3,2] row_mask:0xf bank_mask:0xf bound_ctrl:1
	s_nop 1
	v_add_f32_dpp v170, v170, v170 quad_perm:[2,3,0,1] row_mask:0xf bank_mask:0xf bound_ctrl:1
	s_nop 1
	v_add_f32_dpp v170, v170, v170 row_half_mirror row_mask:0xf bank_mask:0xf bound_ctrl:1
	s_nop 1
	v_add_f32_dpp v170, v170, v170 row_mirror row_mask:0xf bank_mask:0xf bound_ctrl:1
	ds_bpermute_b32 v172, v172, v170
	s_waitcnt lgkmcnt(0)
	v_add_f32_e32 v172, v170, v172
	v_mov_b32_e32 v170, v172
	s_nop 1
	v_permlane32_swap_b32 v172, v170
	s_nop 0
	v_pk_add_f32 v[170:171], v[172:173], v[170:171]
	v_mov_b32_e32 v172, 0x358637bd
	v_pk_fma_f32 v[170:171], v[170:171], s[12:13], v[172:173] op_sel_hi:[1,0,0]
	s_nop 0
	v_mul_f32_e32 v172, 0x4b800000, v171
	v_cmp_gt_f32_e32 vcc, s59, v171
	v_cmp_gt_f32_e64 s[12:13], s59, v170
	s_nop 0
	v_cndmask_b32_e32 v171, v171, v172, vcc
	v_mul_f32_e32 v172, 0x4b800000, v170
	v_rsq_f32_e32 v171, v171
	v_cndmask_b32_e64 v170, v170, v172, s[12:13]
	v_rsq_f32_e32 v172, v170
	v_mul_f32_e32 v170, 0x45800000, v171
	v_cndmask_b32_e32 v170, v171, v170, vcc
	v_mul_f32_e32 v171, 0x45800000, v172
	v_cndmask_b32_e64 v172, v172, v171, s[12:13]
	v_pk_mul_f32 v[130:131], v[172:173], v[130:131] op_sel_hi:[0,1]
	v_pk_fma_f32 v[174:175], v[92:93], v[130:131], v[76:77]
	v_mov_b32_e32 v131, v136
	v_mov_b32_e32 v136, v157
	v_mov_b32_e32 v157, v132
	v_mov_b32_e32 v132, v165
	v_pk_mul_f32 v[132:133], v[172:173], v[132:133] op_sel_hi:[0,1]
	v_pk_mul_f32 v[126:127], v[170:171], v[126:127] op_sel_hi:[0,1]
	v_pk_mul_f32 v[122:123], v[172:173], v[122:123] op_sel_hi:[0,1]
	v_mov_b32_e32 v130, v156
	v_mov_b32_e32 v156, v164
	v_pk_fma_f32 v[164:165], v[96:97], v[132:133], v[80:81]
	v_pk_mul_f32 v[132:133], v[170:171], v[158:159] op_sel_hi:[0,1]
	v_pk_fma_f32 v[158:159], v[100:101], v[126:127], v[84:85]
	v_pk_mul_f32 v[126:127], v[172:173], v[166:167] op_sel_hi:[0,1]
	v_pk_fma_f32 v[166:167], v[100:101], v[122:123], v[84:85]
	v_pk_mul_f32 v[122:123], v[170:171], v[160:161] op_sel_hi:[0,1]
	v_pk_mul_f32 v[154:155], v[170:171], v[154:155] op_sel_hi:[0,1]
	v_pk_mul_f32 v[134:135], v[170:171], v[134:135] op_sel_hi:[0,1]
	v_pk_mul_f32 v[130:131], v[170:171], v[130:131] op_sel_hi:[0,1]
	v_pk_mul_f32 v[136:137], v[170:171], v[136:137] op_sel_hi:[0,1]
	v_pk_fma_f32 v[176:177], v[98:99], v[126:127], v[82:83]
	v_pk_mul_f32 v[126:127], v[170:171], v[128:129] op_sel_hi:[0,1]
	v_pk_fma_f32 v[170:171], v[102:103], v[122:123], v[86:87]
	v_pk_mul_f32 v[122:123], v[172:173], v[168:169] op_sel_hi:[0,1]
	v_pk_mul_f32 v[124:125], v[172:173], v[124:125] op_sel_hi:[0,1]
	v_pk_fma_f32 v[154:155], v[90:91], v[154:155], v[74:75]
	v_pk_mul_f32 v[162:163], v[172:173], v[162:163] op_sel_hi:[0,1]
	v_pk_fma_f32 v[130:131], v[94:95], v[130:131], v[78:79]
	v_pk_mul_f32 v[156:157], v[172:173], v[156:157] op_sel_hi:[0,1]
	v_pk_fma_f32 v[132:133], v[98:99], v[132:133], v[82:83]
	v_pk_fma_f32 v[168:169], v[104:105], v[124:125], v[88:89]
	v_pk_fma_f32 v[172:173], v[102:103], v[122:123], v[86:87]
	v_cvt_pk_fp8_f32 v122, v154, v155
	v_cvt_pk_fp8_f32 v123, v130, v131
	v_cvt_pk_fp8_f32 v124, v132, v133
	v_cvt_pk_fp8_f32 v125, v170, v171
	v_pk_fma_f32 v[134:135], v[92:93], v[134:135], v[76:77]
	v_pk_fma_f32 v[136:137], v[96:97], v[136:137], v[80:81]
	v_pk_fma_f32 v[160:161], v[104:105], v[126:127], v[88:89]
	v_cvt_pk_fp8_f32 v122, v134, v135 op_sel:[0,0,1]
	v_cvt_pk_fp8_f32 v123, v136, v137 op_sel:[0,0,1]
	v_cvt_pk_fp8_f32 v124, v158, v159 op_sel:[0,0,1]
	v_cvt_pk_fp8_f32 v125, v160, v161 op_sel:[0,0,1]
	s_lshl_b64 s[12:13], s[16:17], 10
	v_lshl_add_u64 v[126:127], v[142:143], 0, s[12:13]
	v_pk_fma_f32 v[162:163], v[90:91], v[162:163], v[74:75]
	global_store_dwordx4 v[126:127], v[122:125], off
	v_pk_fma_f32 v[156:157], v[94:95], v[156:157], v[78:79]
	s_or_b32 s12, s16, 1
	v_cvt_pk_bf16_f32 v122, v154, v155
	v_lshlrev_b32_e32 v124, 16, v122
	v_and_b32_e32 v125, 0xffff0000, v122
	v_pk_add_f32 v[124:125], v[154:155], v[124:125] neg_lo:[0,1] neg_hi:[0,1]
	v_cvt_pk_bf16_f32 v123, v134, v135
	v_cvt_pk_bf16_f32 v126, v124, v125
	v_lshlrev_b32_e32 v124, 16, v123
	v_and_b32_e32 v125, 0xffff0000, v123
	v_pk_add_f32 v[124:125], v[134:135], v[124:125] neg_lo:[0,1] neg_hi:[0,1]
	s_ashr_i32 s13, s12, 31
	v_cvt_pk_bf16_f32 v127, v124, v125
	v_cvt_pk_bf16_f32 v124, v130, v131
	v_lshlrev_b32_e32 v128, 16, v124
	v_and_b32_e32 v129, 0xffff0000, v124
	v_cvt_pk_bf16_f32 v125, v136, v137
	v_pk_add_f32 v[128:129], v[130:131], v[128:129] neg_lo:[0,1] neg_hi:[0,1]
	v_lshlrev_b32_e32 v130, 16, v125
	v_and_b32_e32 v131, 0xffff0000, v125
	v_pk_add_f32 v[130:131], v[136:137], v[130:131] neg_lo:[0,1] neg_hi:[0,1]
	v_cvt_pk_bf16_f32 v128, v128, v129
	v_cvt_pk_bf16_f32 v129, v130, v131
	v_cvt_pk_bf16_f32 v130, v132, v133
	v_lshlrev_b32_e32 v134, 16, v130
	v_and_b32_e32 v135, 0xffff0000, v130
	v_pk_add_f32 v[132:133], v[132:133], v[134:135] neg_lo:[0,1] neg_hi:[0,1]
	v_cvt_pk_bf16_f32 v131, v158, v159
	v_cvt_pk_bf16_f32 v134, v132, v133
	v_lshlrev_b32_e32 v132, 16, v131
	v_and_b32_e32 v133, 0xffff0000, v131
	v_pk_add_f32 v[132:133], v[158:159], v[132:133] neg_lo:[0,1] neg_hi:[0,1]
	s_lshl_b64 s[12:13], s[12:13], 10
	v_cvt_pk_bf16_f32 v135, v132, v133
	v_cvt_pk_bf16_f32 v132, v170, v171
	v_cvt_pk_bf16_f32 v133, v160, v161
	v_lshlrev_b32_e32 v136, 16, v132
	v_and_b32_e32 v137, 0xffff0000, v132
	v_lshlrev_b32_e32 v154, 16, v133
	v_and_b32_e32 v155, 0xffff0000, v133
	v_pk_add_f32 v[136:137], v[170:171], v[136:137] neg_lo:[0,1] neg_hi:[0,1]
	v_pk_add_f32 v[154:155], v[160:161], v[154:155] neg_lo:[0,1] neg_hi:[0,1]
	v_cvt_pk_bf16_f32 v136, v136, v137
	v_cvt_pk_bf16_f32 v137, v154, v155
	v_add_u32_e32 v154, s23, v149
	ds_write_b128 v154, v[122:125]
	ds_write_b128 v154, v[130:133] offset:16
	ds_write_b128 v154, v[126:129] offset:33024
	ds_write_b128 v154, v[134:137] offset:33040
	s_nop 0
	s_nop 0
	s_nop 0
	s_nop 0
	v_cvt_pk_fp8_f32 v122, v162, v163
	v_cvt_pk_fp8_f32 v123, v156, v157
	v_cvt_pk_fp8_f32 v124, v176, v177
	v_cvt_pk_fp8_f32 v125, v172, v173
	v_cvt_pk_fp8_f32 v122, v174, v175 op_sel:[0,0,1]
	v_cvt_pk_fp8_f32 v123, v164, v165 op_sel:[0,0,1]
	v_cvt_pk_fp8_f32 v124, v166, v167 op_sel:[0,0,1]
	v_cvt_pk_fp8_f32 v125, v168, v169 op_sel:[0,0,1]
	v_lshl_add_u64 v[126:127], v[142:143], 0, s[12:13]
	v_cmp_lt_i32_e32 vcc, -1, v153
	global_store_dwordx4 v[126:127], v[122:125], off
	s_nop 1
	v_cvt_pk_bf16_f32 v122, v162, v163
	v_lshlrev_b32_e32 v124, 16, v122
	v_and_b32_e32 v125, 0xffff0000, v122
	v_pk_add_f32 v[124:125], v[162:163], v[124:125] neg_lo:[0,1] neg_hi:[0,1]
	v_cvt_pk_bf16_f32 v123, v174, v175
	v_cvt_pk_bf16_f32 v126, v124, v125
	v_lshlrev_b32_e32 v124, 16, v123
	v_and_b32_e32 v125, 0xffff0000, v123
	v_pk_add_f32 v[124:125], v[174:175], v[124:125] neg_lo:[0,1] neg_hi:[0,1]
	s_nop 0
	v_cvt_pk_bf16_f32 v127, v124, v125
	v_cvt_pk_bf16_f32 v124, v156, v157
	v_cvt_pk_bf16_f32 v125, v164, v165
	v_lshlrev_b32_e32 v128, 16, v124
	v_and_b32_e32 v129, 0xffff0000, v124
	v_lshlrev_b32_e32 v130, 16, v125
	v_and_b32_e32 v131, 0xffff0000, v125
	v_pk_add_f32 v[128:129], v[156:157], v[128:129] neg_lo:[0,1] neg_hi:[0,1]
	v_pk_add_f32 v[130:131], v[164:165], v[130:131] neg_lo:[0,1] neg_hi:[0,1]
	v_cvt_pk_bf16_f32 v128, v128, v129
	v_cvt_pk_bf16_f32 v129, v130, v131
	v_cvt_pk_bf16_f32 v130, v176, v177
	v_lshlrev_b32_e32 v132, 16, v130
	v_and_b32_e32 v133, 0xffff0000, v130
	v_pk_add_f32 v[132:133], v[176:177], v[132:133] neg_lo:[0,1] neg_hi:[0,1]
	v_cvt_pk_bf16_f32 v131, v166, v167
	v_cvt_pk_bf16_f32 v134, v132, v133
	v_lshlrev_b32_e32 v132, 16, v131
	v_and_b32_e32 v133, 0xffff0000, v131
	v_pk_add_f32 v[132:133], v[166:167], v[132:133] neg_lo:[0,1] neg_hi:[0,1]
	s_nop 0
	v_cvt_pk_bf16_f32 v135, v132, v133
	v_cvt_pk_bf16_f32 v132, v172, v173
	v_cvt_pk_bf16_f32 v133, v168, v169
	v_lshlrev_b32_e32 v136, 16, v132
	v_and_b32_e32 v137, 0xffff0000, v132
	v_lshlrev_b32_e32 v154, 16, v133
	v_and_b32_e32 v155, 0xffff0000, v133
	v_pk_add_f32 v[136:137], v[172:173], v[136:137] neg_lo:[0,1] neg_hi:[0,1]
	v_pk_add_f32 v[154:155], v[168:169], v[154:155] neg_lo:[0,1] neg_hi:[0,1]
	v_cvt_pk_bf16_f32 v136, v136, v137
	v_cvt_pk_bf16_f32 v137, v154, v155
	v_add_u32_e32 v154, s24, v149
	ds_write_b128 v154, v[122:125]
	ds_write_b128 v154, v[130:133] offset:16
	ds_write_b128 v154, v[126:129] offset:33024
	ds_write_b128 v154, v[134:137] offset:33040
	s_and_saveexec_b64 s[12:13], vcc
	s_cbranch_execz .LBB0_1549
	s_mov_b32 s14, 35
	s_ashr_i32 s15, s14, 31
	s_lshl_b64 s[14:15], s[14:15], 3
	s_add_u32 s14, s0, s14
	s_addc_u32 s15, s1, s15
	s_load_dwordx2 s[14:15], s[14:15], 0x0
	v_lshlrev_b32_e32 v122, 2, v153
	v_mov_b32_e32 v123, v1
	v_lshlrev_b64 v[122:123], 2, v[122:123]
	v_mov_b32_e32 v153, -1
	s_waitcnt lgkmcnt(0)
	v_lshl_add_u64 v[124:125], s[14:15], 0, v[122:123]
	v_add_co_u32_e32 v124, vcc, s85, v124
	s_mov_b32 s14, 35
	s_nop 0
	v_addc_co_u32_e32 v125, vcc, 0, v125, vcc
	global_store_dwordx4 v[124:125], v[70:73], off
	s_ashr_i32 s15, s14, 31
	s_lshl_b64 s[14:15], s[14:15], 3
	s_add_u32 s14, s0, s14
	s_addc_u32 s15, s1, s15
	s_load_dwordx2 s[14:15], s[14:15], 0x0
	s_waitcnt lgkmcnt(0)
	v_lshl_add_u64 v[122:123], s[14:15], 0, v[122:123]
	v_add_co_u32_e32 v122, vcc, 0xa00000, v122
	s_nop 1
	v_addc_co_u32_e32 v123, vcc, 0, v123, vcc
	global_store_dwordx4 v[122:123], v[66:69], off

.LBB0_1791:
	v_add_u32_e32 v0, s67, v185
	ds_read_b128 v[10:13], v0
	ds_read_b128 v[2:5], v0 offset:16
	ds_read_b128 v[14:17], v0 offset:512
	ds_read_b128 v[6:9], v0 offset:528
	v_lshl_or_b32 v0, s66, 7, v183
	s_waitcnt lgkmcnt(0)
	v_pk_add_f32 v[20:21], v[158:159], v[10:11]
	v_pk_add_f32 v[18:19], v[160:161], v[12:13]
	v_min_f32_e32 v20, 0x40e00000, v20
	v_min_f32_e32 v21, 0x40e00000, v21
	v_pk_mul_f32 v[26:27], v[20:21], s[88:89] op_sel_hi:[1,0]
	v_pk_add_f32 v[24:25], v[154:155], v[14:15]
	v_exp_f32_e32 v26, v26
	v_exp_f32_e32 v27, v27
	v_mov_b32_e32 v154, 0x40e00000
	v_med3_f32 v24, v24, s72, v154
	v_med3_f32 v25, v25, s72, v154
	v_pk_add_f32 v[26:27], v[26:27], 1.0 op_sel_hi:[1,0]
	v_pk_add_f32 v[24:25], v[24:25], 1.0 op_sel_hi:[1,0]
	v_rcp_f32_e32 v26, v26
	v_rcp_f32_e32 v27, v27
	v_min_f32_e32 v18, 0x40e00000, v18
	v_min_f32_e32 v19, 0x40e00000, v19
	v_pk_add_f32 v[22:23], v[156:157], v[16:17]
	v_pk_mul_f32 v[20:21], v[20:21], v[26:27]
	v_med3_f32 v22, v22, s72, v154
	v_pk_mul_f32 v[20:21], v[24:25], v[20:21]
	v_pk_mul_f32 v[24:25], v[18:19], s[88:89] op_sel_hi:[1,0]
	v_med3_f32 v23, v23, s72, v154
	v_exp_f32_e32 v24, v24
	v_exp_f32_e32 v25, v25
	v_pk_add_f32 v[22:23], v[22:23], 1.0 op_sel_hi:[1,0]
	v_pk_add_f32 v[28:29], v[146:147], v[6:7]
	v_pk_add_f32 v[26:27], v[148:149], v[8:9]
	v_pk_add_f32 v[24:25], v[24:25], 1.0 op_sel_hi:[1,0]
	v_med3_f32 v28, v28, s72, v154
	v_rcp_f32_e32 v24, v24
	v_rcp_f32_e32 v25, v25
	v_med3_f32 v29, v29, s72, v154
	v_pk_add_f32 v[28:29], v[28:29], 1.0 op_sel_hi:[1,0]
	v_med3_f32 v26, v26, s72, v154
	v_pk_mul_f32 v[18:19], v[18:19], v[24:25]
	v_pk_add_f32 v[24:25], v[150:151], v[2:3]
	v_pk_mul_f32 v[22:23], v[22:23], v[18:19]
	v_min_f32_e32 v24, 0x40e00000, v24
	v_min_f32_e32 v25, 0x40e00000, v25
	v_pk_mul_f32 v[30:31], v[24:25], s[88:89] op_sel_hi:[1,0]
	v_pk_add_f32 v[18:19], v[152:153], v[4:5]
	v_exp_f32_e32 v30, v30
	v_exp_f32_e32 v31, v31
	v_min_f32_e32 v18, 0x40e00000, v18
	v_min_f32_e32 v19, 0x40e00000, v19
	v_med3_f32 v27, v27, s72, v154
	v_pk_add_f32 v[30:31], v[30:31], 1.0 op_sel_hi:[1,0]
	v_pk_add_f32 v[26:27], v[26:27], 1.0 op_sel_hi:[1,0]
	v_rcp_f32_e32 v30, v30
	v_rcp_f32_e32 v31, v31
	s_mov_b64 s[18:19], -1
	s_andn2_b64 vcc, exec, s[16:17]
	s_mov_b32 s69, s50
	v_pk_mul_f32 v[24:25], v[24:25], v[30:31]
	v_pk_add_f32 v[30:31], v[130:131], v[6:7]
	v_pk_mul_f32 v[24:25], v[28:29], v[24:25]
	v_pk_mul_f32 v[28:29], v[18:19], s[88:89] op_sel_hi:[1,0]
	v_med3_f32 v30, v30, s72, v154
	v_exp_f32_e32 v28, v28
	v_exp_f32_e32 v29, v29
	v_med3_f32 v31, v31, s72, v154
	v_pk_add_f32 v[30:31], v[30:31], 1.0 op_sel_hi:[1,0]
	s_mov_b32 s68, s86
	v_pk_add_f32 v[28:29], v[28:29], 1.0 op_sel_hi:[1,0]
	s_nop 0
	v_rcp_f32_e32 v28, v28
	v_rcp_f32_e32 v29, v29
	s_nop 0
	v_pk_mul_f32 v[18:19], v[18:19], v[28:29]
	s_nop 0
	v_pk_mul_f32 v[26:27], v[26:27], v[18:19]
	v_cvt_pk_fp8_f32 v18, v20, v21
	v_cvt_pk_fp8_f32 v19, v24, v25
	v_pk_add_f32 v[20:21], v[144:145], v[12:13]
	v_cvt_pk_fp8_f32 v18, v22, v23 op_sel:[0,0,1]
	v_pk_add_f32 v[22:23], v[142:143], v[10:11]
	v_cvt_pk_fp8_f32 v19, v26, v27 op_sel:[0,0,1]
	v_min_f32_e32 v22, 0x40e00000, v22
	v_min_f32_e32 v23, 0x40e00000, v23
	v_pk_mul_f32 v[28:29], v[22:23], s[88:89] op_sel_hi:[1,0]
	v_pk_add_f32 v[26:27], v[138:139], v[14:15]
	v_exp_f32_e32 v28, v28
	v_exp_f32_e32 v29, v29
	v_med3_f32 v26, v26, s72, v154
	v_med3_f32 v27, v27, s72, v154
	v_pk_add_f32 v[26:27], v[26:27], 1.0 op_sel_hi:[1,0]
	v_pk_add_f32 v[28:29], v[28:29], 1.0 op_sel_hi:[1,0]
	v_min_f32_e32 v20, 0x40e00000, v20
	v_rcp_f32_e32 v28, v28
	v_rcp_f32_e32 v29, v29
	v_min_f32_e32 v21, 0x40e00000, v21
	v_pk_add_f32 v[24:25], v[140:141], v[16:17]
	v_pk_mul_f32 v[22:23], v[22:23], v[28:29]
	s_nop 0
	v_pk_mul_f32 v[22:23], v[26:27], v[22:23]
	v_pk_mul_f32 v[26:27], v[20:21], s[88:89] op_sel_hi:[1,0]
	v_med3_f32 v24, v24, s72, v154
	v_exp_f32_e32 v26, v26
	v_exp_f32_e32 v27, v27
	v_med3_f32 v25, v25, s72, v154
	v_pk_add_f32 v[24:25], v[24:25], 1.0 op_sel_hi:[1,0]
	v_pk_add_f32 v[28:29], v[132:133], v[8:9]
	v_pk_add_f32 v[26:27], v[26:27], 1.0 op_sel_hi:[1,0]
	v_med3_f32 v28, v28, s72, v154
	v_rcp_f32_e32 v26, v26
	v_rcp_f32_e32 v27, v27
	v_med3_f32 v29, v29, s72, v154
	v_pk_add_f32 v[28:29], v[28:29], 1.0 op_sel_hi:[1,0]
	v_pk_mul_f32 v[20:21], v[20:21], v[26:27]
	v_pk_add_f32 v[26:27], v[134:135], v[2:3]
	v_pk_mul_f32 v[24:25], v[24:25], v[20:21]
	v_min_f32_e32 v26, 0x40e00000, v26
	v_min_f32_e32 v27, 0x40e00000, v27
	v_pk_mul_f32 v[32:33], v[26:27], s[88:89] op_sel_hi:[1,0]
	v_pk_add_f32 v[20:21], v[136:137], v[4:5]
	v_exp_f32_e32 v32, v32
	v_exp_f32_e32 v33, v33
	v_min_f32_e32 v20, 0x40e00000, v20
	v_min_f32_e32 v21, 0x40e00000, v21
	v_pk_add_f32 v[32:33], v[32:33], 1.0 op_sel_hi:[1,0]
	s_nop 0
	v_rcp_f32_e32 v32, v32
	v_rcp_f32_e32 v33, v33
	s_nop 0
	v_pk_mul_f32 v[26:27], v[26:27], v[32:33]
	s_nop 0
	v_pk_mul_f32 v[26:27], v[30:31], v[26:27]
	v_pk_mul_f32 v[30:31], v[20:21], s[88:89] op_sel_hi:[1,0]
	s_nop 0
	v_exp_f32_e32 v30, v30
	v_exp_f32_e32 v31, v31
	s_nop 0
	v_pk_add_f32 v[30:31], v[30:31], 1.0 op_sel_hi:[1,0]
	s_nop 0
	v_rcp_f32_e32 v30, v30
	v_rcp_f32_e32 v31, v31
	s_nop 0
	v_pk_mul_f32 v[20:21], v[20:21], v[30:31]
	s_nop 0
	v_pk_mul_f32 v[28:29], v[28:29], v[20:21]
	v_cvt_pk_fp8_f32 v20, v22, v23
	v_cvt_pk_fp8_f32 v21, v26, v27
	v_lshl_add_u32 v22, s62, 18, v184
	v_or_b32_e32 v23, v22, v0
	v_cvt_pk_fp8_f32 v20, v24, v25 op_sel:[0,0,1]
	v_cvt_pk_fp8_f32 v21, v28, v29 op_sel:[0,0,1]
	s_nop 1
	v_permlane16_swap_b32 v18, v20
	v_pk_add_f32 v[26:27], v[122:123], v[14:15]
	s_nop 1
	v_permlane16_swap_b32 v19, v21
	global_store_dwordx4 v23, v[18:21], s[8:9]
	v_med3_f32 v26, v26, s72, v154
	v_med3_f32 v27, v27, s72, v154
	v_pk_add_f32 v[20:21], v[126:127], v[10:11]
	v_pk_add_f32 v[18:19], v[128:129], v[12:13]
	v_min_f32_e32 v20, 0x40e00000, v20
	v_min_f32_e32 v21, 0x40e00000, v21
	v_pk_mul_f32 v[28:29], v[20:21], s[88:89] op_sel_hi:[1,0]
	v_pk_add_f32 v[26:27], v[26:27], 1.0 op_sel_hi:[1,0]
	v_exp_f32_e32 v28, v28
	v_exp_f32_e32 v29, v29
	v_min_f32_e32 v18, 0x40e00000, v18
	v_min_f32_e32 v19, 0x40e00000, v19
	v_pk_add_f32 v[24:25], v[124:125], v[16:17]
	v_pk_add_f32 v[28:29], v[28:29], 1.0 op_sel_hi:[1,0]
	v_med3_f32 v24, v24, s72, v154
	v_rcp_f32_e32 v28, v28
	v_rcp_f32_e32 v29, v29
	v_med3_f32 v25, v25, s72, v154
	v_pk_add_f32 v[24:25], v[24:25], 1.0 op_sel_hi:[1,0]
	v_pk_add_f32 v[30:31], v[114:115], v[6:7]
	v_pk_mul_f32 v[20:21], v[20:21], v[28:29]
	v_med3_f32 v30, v30, s72, v154
	v_pk_mul_f32 v[20:21], v[26:27], v[20:21]
	v_pk_mul_f32 v[26:27], v[18:19], s[88:89] op_sel_hi:[1,0]
	v_med3_f32 v31, v31, s72, v154
	v_exp_f32_e32 v26, v26
	v_exp_f32_e32 v27, v27
	v_pk_add_f32 v[30:31], v[30:31], 1.0 op_sel_hi:[1,0]
	v_pk_add_f32 v[28:29], v[116:117], v[8:9]
	v_or_b32_e32 v23, 0x8000, v23
	v_pk_add_f32 v[26:27], v[26:27], 1.0 op_sel_hi:[1,0]
	v_med3_f32 v28, v28, s72, v154
	v_rcp_f32_e32 v26, v26
	v_rcp_f32_e32 v27, v27
	v_med3_f32 v29, v29, s72, v154
	v_pk_add_f32 v[28:29], v[28:29], 1.0 op_sel_hi:[1,0]
	v_add_u32_e32 v0, v22, v0
	v_pk_mul_f32 v[18:19], v[18:19], v[26:27]
	v_pk_add_f32 v[26:27], v[118:119], v[2:3]
	v_pk_mul_f32 v[24:25], v[24:25], v[18:19]
	v_min_f32_e32 v26, 0x40e00000, v26
	v_min_f32_e32 v27, 0x40e00000, v27
	v_pk_mul_f32 v[32:33], v[26:27], s[88:89] op_sel_hi:[1,0]
	v_pk_add_f32 v[18:19], v[120:121], v[4:5]
	v_exp_f32_e32 v32, v32
	v_exp_f32_e32 v33, v33
	v_min_f32_e32 v18, 0x40e00000, v18
	v_min_f32_e32 v19, 0x40e00000, v19
	v_add_u32_e32 v22, 0x20000, v0
	v_pk_add_f32 v[32:33], v[32:33], 1.0 op_sel_hi:[1,0]
	v_add_u32_e32 v0, 0x28000, v0
	v_rcp_f32_e32 v32, v32
	v_rcp_f32_e32 v33, v33
	s_nop 0
	v_pk_mul_f32 v[26:27], v[26:27], v[32:33]
	s_nop 0
	v_pk_mul_f32 v[26:27], v[30:31], v[26:27]
	v_pk_mul_f32 v[30:31], v[18:19], s[88:89] op_sel_hi:[1,0]
	v_pk_add_f32 v[32:33], v[98:99], v[6:7]
	v_exp_f32_e32 v30, v30
	v_exp_f32_e32 v31, v31
	v_med3_f32 v32, v32, s72, v154
	v_med3_f32 v33, v33, s72, v154
	v_pk_add_f32 v[32:33], v[32:33], 1.0 op_sel_hi:[1,0]
	v_pk_add_f32 v[30:31], v[30:31], 1.0 op_sel_hi:[1,0]
	s_nop 0
	v_rcp_f32_e32 v30, v30
	v_rcp_f32_e32 v31, v31
	s_nop 0
	v_pk_mul_f32 v[18:19], v[18:19], v[30:31]
	s_nop 0
	v_pk_mul_f32 v[28:29], v[28:29], v[18:19]
	v_cvt_pk_fp8_f32 v18, v20, v21
	v_cvt_pk_fp8_f32 v19, v26, v27
	v_pk_add_f32 v[20:21], v[112:113], v[12:13]
	v_cvt_pk_fp8_f32 v18, v24, v25 op_sel:[0,0,1]
	v_pk_add_f32 v[24:25], v[110:111], v[10:11]
	v_cvt_pk_fp8_f32 v19, v28, v29 op_sel:[0,0,1]
	v_min_f32_e32 v24, 0x40e00000, v24
	v_min_f32_e32 v25, 0x40e00000, v25
	v_pk_mul_f32 v[30:31], v[24:25], s[88:89] op_sel_hi:[1,0]
	v_pk_add_f32 v[28:29], v[106:107], v[14:15]
	v_exp_f32_e32 v30, v30
	v_exp_f32_e32 v31, v31
	v_med3_f32 v28, v28, s72, v154
	v_med3_f32 v29, v29, s72, v154
	v_pk_add_f32 v[28:29], v[28:29], 1.0 op_sel_hi:[1,0]
	v_pk_add_f32 v[30:31], v[30:31], 1.0 op_sel_hi:[1,0]
	v_min_f32_e32 v20, 0x40e00000, v20
	v_rcp_f32_e32 v30, v30
	v_rcp_f32_e32 v31, v31
	v_min_f32_e32 v21, 0x40e00000, v21
	v_pk_add_f32 v[26:27], v[108:109], v[16:17]
	v_pk_mul_f32 v[24:25], v[24:25], v[30:31]
	s_nop 0
	v_pk_mul_f32 v[24:25], v[28:29], v[24:25]
	v_pk_mul_f32 v[28:29], v[20:21], s[88:89] op_sel_hi:[1,0]
	v_med3_f32 v26, v26, s72, v154
	v_exp_f32_e32 v28, v28
	v_exp_f32_e32 v29, v29
	v_med3_f32 v27, v27, s72, v154
	v_pk_add_f32 v[26:27], v[26:27], 1.0 op_sel_hi:[1,0]
	v_pk_add_f32 v[30:31], v[100:101], v[8:9]
	v_pk_add_f32 v[28:29], v[28:29], 1.0 op_sel_hi:[1,0]
	v_med3_f32 v30, v30, s72, v154
	v_rcp_f32_e32 v28, v28
	v_rcp_f32_e32 v29, v29
	v_med3_f32 v31, v31, s72, v154
	v_pk_add_f32 v[30:31], v[30:31], 1.0 op_sel_hi:[1,0]
	v_pk_mul_f32 v[20:21], v[20:21], v[28:29]
	v_pk_add_f32 v[28:29], v[102:103], v[2:3]
	v_pk_mul_f32 v[26:27], v[26:27], v[20:21]
	v_min_f32_e32 v28, 0x40e00000, v28
	v_min_f32_e32 v29, 0x40e00000, v29
	v_pk_mul_f32 v[98:99], v[28:29], s[88:89] op_sel_hi:[1,0]
	v_pk_add_f32 v[20:21], v[104:105], v[4:5]
	v_exp_f32_e32 v98, v98
	v_exp_f32_e32 v99, v99
	v_min_f32_e32 v20, 0x40e00000, v20
	v_min_f32_e32 v21, 0x40e00000, v21
	v_pk_add_f32 v[98:99], v[98:99], 1.0 op_sel_hi:[1,0]
	s_nop 0
	v_rcp_f32_e32 v98, v98
	v_rcp_f32_e32 v99, v99
	s_nop 0
	v_pk_mul_f32 v[28:29], v[28:29], v[98:99]
	s_nop 0
	v_pk_mul_f32 v[28:29], v[32:33], v[28:29]
	v_pk_mul_f32 v[32:33], v[20:21], s[88:89] op_sel_hi:[1,0]
	s_nop 0
	v_exp_f32_e32 v32, v32
	v_exp_f32_e32 v33, v33
	s_nop 0
	v_pk_add_f32 v[32:33], v[32:33], 1.0 op_sel_hi:[1,0]
	s_nop 0
	v_rcp_f32_e32 v32, v32
	v_rcp_f32_e32 v33, v33
	s_nop 0
	v_pk_mul_f32 v[20:21], v[20:21], v[32:33]
	s_nop 0
	v_pk_mul_f32 v[30:31], v[30:31], v[20:21]
	v_cvt_pk_fp8_f32 v20, v24, v25
	v_cvt_pk_fp8_f32 v21, v28, v29
	v_pk_add_f32 v[24:25], v[92:93], v[16:17]
	v_cvt_pk_fp8_f32 v20, v26, v27 op_sel:[0,0,1]
	v_cvt_pk_fp8_f32 v21, v30, v31 op_sel:[0,0,1]
	s_nop 1
	v_permlane16_swap_b32 v18, v20
	v_pk_add_f32 v[26:27], v[90:91], v[14:15]
	s_nop 1
	v_permlane16_swap_b32 v19, v21
	global_store_dwordx4 v23, v[18:21], s[8:9]
	v_med3_f32 v26, v26, s72, v154
	v_med3_f32 v27, v27, s72, v154
	v_pk_add_f32 v[20:21], v[94:95], v[10:11]
	v_pk_add_f32 v[18:19], v[96:97], v[12:13]
	v_min_f32_e32 v20, 0x40e00000, v20
	v_min_f32_e32 v21, 0x40e00000, v21
	v_pk_mul_f32 v[28:29], v[20:21], s[88:89] op_sel_hi:[1,0]
	v_pk_add_f32 v[26:27], v[26:27], 1.0 op_sel_hi:[1,0]
	v_exp_f32_e32 v28, v28
	v_exp_f32_e32 v29, v29
	v_min_f32_e32 v18, 0x40e00000, v18
	v_min_f32_e32 v19, 0x40e00000, v19
	v_med3_f32 v24, v24, s72, v154
	v_pk_add_f32 v[28:29], v[28:29], 1.0 op_sel_hi:[1,0]
	v_med3_f32 v25, v25, s72, v154
	v_rcp_f32_e32 v28, v28
	v_rcp_f32_e32 v29, v29
	v_pk_add_f32 v[24:25], v[24:25], 1.0 op_sel_hi:[1,0]
	v_pk_add_f32 v[30:31], v[82:83], v[6:7]
	v_pk_mul_f32 v[20:21], v[20:21], v[28:29]
	s_nop 0
	v_pk_mul_f32 v[20:21], v[26:27], v[20:21]
	v_pk_mul_f32 v[26:27], v[18:19], s[88:89] op_sel_hi:[1,0]
	v_med3_f32 v30, v30, s72, v154
	v_exp_f32_e32 v26, v26
	v_exp_f32_e32 v27, v27
	v_med3_f32 v31, v31, s72, v154
	v_pk_add_f32 v[30:31], v[30:31], 1.0 op_sel_hi:[1,0]
	v_pk_add_f32 v[28:29], v[84:85], v[8:9]
	v_pk_add_f32 v[26:27], v[26:27], 1.0 op_sel_hi:[1,0]
	v_med3_f32 v28, v28, s72, v154
	v_rcp_f32_e32 v26, v26
	v_rcp_f32_e32 v27, v27
	v_med3_f32 v29, v29, s72, v154
	v_pk_add_f32 v[28:29], v[28:29], 1.0 op_sel_hi:[1,0]
	v_pk_mul_f32 v[18:19], v[18:19], v[26:27]
	v_pk_add_f32 v[26:27], v[86:87], v[2:3]
	v_pk_mul_f32 v[24:25], v[24:25], v[18:19]
	v_min_f32_e32 v26, 0x40e00000, v26
	v_min_f32_e32 v27, 0x40e00000, v27
	v_pk_mul_f32 v[32:33], v[26:27], s[88:89] op_sel_hi:[1,0]
	v_pk_add_f32 v[18:19], v[88:89], v[4:5]
	v_exp_f32_e32 v32, v32
	v_exp_f32_e32 v33, v33
	v_min_f32_e32 v18, 0x40e00000, v18
	v_min_f32_e32 v19, 0x40e00000, v19
	v_pk_add_f32 v[32:33], v[32:33], 1.0 op_sel_hi:[1,0]
	s_nop 0
	v_rcp_f32_e32 v32, v32
	v_rcp_f32_e32 v33, v33
	s_nop 0
	v_pk_mul_f32 v[26:27], v[26:27], v[32:33]
	s_nop 0
	v_pk_mul_f32 v[26:27], v[30:31], v[26:27]
	v_pk_mul_f32 v[30:31], v[18:19], s[88:89] op_sel_hi:[1,0]
	v_pk_add_f32 v[32:33], v[66:67], v[6:7]
	v_exp_f32_e32 v30, v30
	v_exp_f32_e32 v31, v31
	v_med3_f32 v32, v32, s72, v154
	v_med3_f32 v33, v33, s72, v154
	v_pk_add_f32 v[32:33], v[32:33], 1.0 op_sel_hi:[1,0]
	v_pk_add_f32 v[30:31], v[30:31], 1.0 op_sel_hi:[1,0]
	s_nop 0
	v_rcp_f32_e32 v30, v30
	v_rcp_f32_e32 v31, v31
	s_nop 0
	v_pk_mul_f32 v[18:19], v[18:19], v[30:31]
	s_nop 0
	v_pk_mul_f32 v[28:29], v[28:29], v[18:19]
	v_cvt_pk_fp8_f32 v18, v20, v21
	v_cvt_pk_fp8_f32 v19, v26, v27
	v_pk_add_f32 v[20:21], v[80:81], v[12:13]
	v_cvt_pk_fp8_f32 v18, v24, v25 op_sel:[0,0,1]
	v_pk_add_f32 v[24:25], v[78:79], v[10:11]
	v_cvt_pk_fp8_f32 v19, v28, v29 op_sel:[0,0,1]
	v_min_f32_e32 v24, 0x40e00000, v24
	v_min_f32_e32 v25, 0x40e00000, v25
	v_pk_mul_f32 v[30:31], v[24:25], s[88:89] op_sel_hi:[1,0]
	v_pk_add_f32 v[28:29], v[74:75], v[14:15]
	v_exp_f32_e32 v30, v30
	v_exp_f32_e32 v31, v31
	v_med3_f32 v28, v28, s72, v154
	v_med3_f32 v29, v29, s72, v154
	v_pk_add_f32 v[28:29], v[28:29], 1.0 op_sel_hi:[1,0]
	v_pk_add_f32 v[30:31], v[30:31], 1.0 op_sel_hi:[1,0]
	v_min_f32_e32 v20, 0x40e00000, v20
	v_rcp_f32_e32 v30, v30
	v_rcp_f32_e32 v31, v31
	v_min_f32_e32 v21, 0x40e00000, v21
	v_pk_add_f32 v[26:27], v[76:77], v[16:17]
	v_pk_mul_f32 v[24:25], v[24:25], v[30:31]
	s_nop 0
	v_pk_mul_f32 v[24:25], v[28:29], v[24:25]
	v_pk_mul_f32 v[28:29], v[20:21], s[88:89] op_sel_hi:[1,0]
	v_med3_f32 v26, v26, s72, v154
	v_exp_f32_e32 v28, v28
	v_exp_f32_e32 v29, v29
	v_med3_f32 v27, v27, s72, v154
	v_pk_add_f32 v[26:27], v[26:27], 1.0 op_sel_hi:[1,0]
	v_pk_add_f32 v[30:31], v[68:69], v[8:9]
	v_pk_add_f32 v[28:29], v[28:29], 1.0 op_sel_hi:[1,0]
	v_med3_f32 v30, v30, s72, v154
	v_rcp_f32_e32 v28, v28
	v_rcp_f32_e32 v29, v29
	v_med3_f32 v31, v31, s72, v154
	v_pk_add_f32 v[30:31], v[30:31], 1.0 op_sel_hi:[1,0]
	v_pk_mul_f32 v[20:21], v[20:21], v[28:29]
	v_pk_add_f32 v[28:29], v[70:71], v[2:3]
	v_pk_mul_f32 v[26:27], v[26:27], v[20:21]
	v_min_f32_e32 v28, 0x40e00000, v28
	v_min_f32_e32 v29, 0x40e00000, v29
	v_pk_mul_f32 v[66:67], v[28:29], s[88:89] op_sel_hi:[1,0]
	v_pk_add_f32 v[20:21], v[72:73], v[4:5]
	v_exp_f32_e32 v66, v66
	v_exp_f32_e32 v67, v67
	v_min_f32_e32 v20, 0x40e00000, v20
	v_min_f32_e32 v21, 0x40e00000, v21
	v_pk_add_f32 v[66:67], v[66:67], 1.0 op_sel_hi:[1,0]
	s_nop 0
	v_rcp_f32_e32 v66, v66
	v_rcp_f32_e32 v67, v67
	s_nop 0
	v_pk_mul_f32 v[28:29], v[28:29], v[66:67]
	s_nop 0
	v_pk_mul_f32 v[28:29], v[32:33], v[28:29]
	v_pk_mul_f32 v[32:33], v[20:21], s[88:89] op_sel_hi:[1,0]
	s_nop 0
	v_exp_f32_e32 v32, v32
	v_exp_f32_e32 v33, v33
	s_nop 0
	v_pk_add_f32 v[32:33], v[32:33], 1.0 op_sel_hi:[1,0]
	s_nop 0
	v_rcp_f32_e32 v32, v32
	v_rcp_f32_e32 v33, v33
	s_nop 0
	v_pk_mul_f32 v[20:21], v[20:21], v[32:33]
	s_nop 0
	v_pk_mul_f32 v[30:31], v[30:31], v[20:21]
	v_cvt_pk_fp8_f32 v20, v24, v25
	v_cvt_pk_fp8_f32 v21, v28, v29
	v_pk_add_f32 v[24:25], v[58:59], v[14:15]
	v_pk_add_f32 v[28:29], v[50:51], v[6:7]
	v_cvt_pk_fp8_f32 v20, v26, v27 op_sel:[0,0,1]
	v_cvt_pk_fp8_f32 v21, v30, v31 op_sel:[0,0,1]
	s_nop 1
	v_permlane16_swap_b32 v18, v20
	v_med3_f32 v24, v24, s72, v154
	s_nop 1
	v_permlane16_swap_b32 v19, v21
	global_store_dwordx4 v22, v[18:21], s[8:9]
	v_med3_f32 v25, v25, s72, v154
	v_pk_add_f32 v[24:25], v[24:25], 1.0 op_sel_hi:[1,0]
	v_pk_add_f32 v[20:21], v[62:63], v[10:11]
	v_pk_add_f32 v[18:19], v[64:65], v[12:13]
	v_min_f32_e32 v20, 0x40e00000, v20
	v_min_f32_e32 v21, 0x40e00000, v21
	v_pk_mul_f32 v[26:27], v[20:21], s[88:89] op_sel_hi:[1,0]
	v_min_f32_e32 v18, 0x40e00000, v18
	v_exp_f32_e32 v26, v26
	v_exp_f32_e32 v27, v27
	v_min_f32_e32 v19, 0x40e00000, v19
	v_pk_add_f32 v[22:23], v[60:61], v[16:17]
	v_med3_f32 v28, v28, s72, v154
	v_pk_add_f32 v[26:27], v[26:27], 1.0 op_sel_hi:[1,0]
	v_med3_f32 v22, v22, s72, v154
	v_rcp_f32_e32 v26, v26
	v_rcp_f32_e32 v27, v27
	v_med3_f32 v23, v23, s72, v154
	v_pk_add_f32 v[22:23], v[22:23], 1.0 op_sel_hi:[1,0]
	v_med3_f32 v29, v29, s72, v154
	v_pk_mul_f32 v[20:21], v[20:21], v[26:27]
	v_pk_add_f32 v[28:29], v[28:29], 1.0 op_sel_hi:[1,0]
	v_pk_mul_f32 v[20:21], v[24:25], v[20:21]
	v_pk_mul_f32 v[24:25], v[18:19], s[88:89] op_sel_hi:[1,0]
	v_pk_add_f32 v[26:27], v[52:53], v[8:9]
	v_exp_f32_e32 v24, v24
	v_exp_f32_e32 v25, v25
	v_med3_f32 v26, v26, s72, v154
	v_med3_f32 v27, v27, s72, v154
	v_pk_add_f32 v[26:27], v[26:27], 1.0 op_sel_hi:[1,0]
	v_pk_add_f32 v[24:25], v[24:25], 1.0 op_sel_hi:[1,0]
	v_pk_add_f32 v[10:11], v[46:47], v[10:11]
	v_rcp_f32_e32 v24, v24
	v_rcp_f32_e32 v25, v25
	v_min_f32_e32 v10, 0x40e00000, v10
	v_min_f32_e32 v11, 0x40e00000, v11
	v_pk_add_f32 v[14:15], v[42:43], v[14:15]
	v_pk_mul_f32 v[18:19], v[18:19], v[24:25]
	v_pk_add_f32 v[24:25], v[54:55], v[2:3]
	v_pk_mul_f32 v[22:23], v[22:23], v[18:19]
	v_min_f32_e32 v24, 0x40e00000, v24
	v_min_f32_e32 v25, 0x40e00000, v25
	v_pk_mul_f32 v[30:31], v[24:25], s[88:89] op_sel_hi:[1,0]
	v_pk_add_f32 v[18:19], v[56:57], v[4:5]
	v_exp_f32_e32 v30, v30
	v_exp_f32_e32 v31, v31
	v_min_f32_e32 v18, 0x40e00000, v18
	v_min_f32_e32 v19, 0x40e00000, v19
	v_pk_add_f32 v[12:13], v[48:49], v[12:13]
	v_pk_add_f32 v[30:31], v[30:31], 1.0 op_sel_hi:[1,0]
	v_med3_f32 v14, v14, s72, v154
	v_rcp_f32_e32 v30, v30
	v_rcp_f32_e32 v31, v31
	v_med3_f32 v15, v15, s72, v154
	v_pk_add_f32 v[16:17], v[44:45], v[16:17]
	v_pk_add_f32 v[14:15], v[14:15], 1.0 op_sel_hi:[1,0]
	v_pk_mul_f32 v[24:25], v[24:25], v[30:31]
	v_min_f32_e32 v12, 0x40e00000, v12
	v_pk_mul_f32 v[24:25], v[28:29], v[24:25]
	v_pk_mul_f32 v[28:29], v[18:19], s[88:89] op_sel_hi:[1,0]
	v_min_f32_e32 v13, 0x40e00000, v13
	v_exp_f32_e32 v28, v28
	v_exp_f32_e32 v29, v29
	v_pk_add_f32 v[2:3], v[38:39], v[2:3]
	v_pk_add_f32 v[6:7], v[34:35], v[6:7]
	v_min_f32_e32 v2, 0x40e00000, v2
	v_pk_add_f32 v[28:29], v[28:29], 1.0 op_sel_hi:[1,0]
	v_min_f32_e32 v3, 0x40e00000, v3
	v_rcp_f32_e32 v28, v28
	v_rcp_f32_e32 v29, v29
	v_pk_add_f32 v[4:5], v[40:41], v[4:5]
	v_med3_f32 v6, v6, s72, v154
	v_med3_f32 v7, v7, s72, v154
	v_pk_mul_f32 v[18:19], v[18:19], v[28:29]
	v_pk_add_f32 v[8:9], v[36:37], v[8:9]
	v_pk_mul_f32 v[26:27], v[26:27], v[18:19]
	s_nop 0
	v_cvt_pk_fp8_f32 v18, v20, v21
	v_pk_mul_f32 v[20:21], v[10:11], s[88:89] op_sel_hi:[1,0]
	v_pk_add_f32 v[6:7], v[6:7], 1.0 op_sel_hi:[1,0]
	v_exp_f32_e32 v20, v20
	v_exp_f32_e32 v21, v21
	v_min_f32_e32 v4, 0x40e00000, v4
	v_min_f32_e32 v5, 0x40e00000, v5
	s_nop 0
	v_pk_add_f32 v[20:21], v[20:21], 1.0 op_sel_hi:[1,0]
	v_cvt_pk_fp8_f32 v19, v24, v25
	v_rcp_f32_e32 v20, v20
	v_rcp_f32_e32 v21, v21
	v_cvt_pk_fp8_f32 v18, v22, v23 op_sel:[0,0,1]
	v_cvt_pk_fp8_f32 v19, v26, v27 op_sel:[0,0,1]
	v_pk_mul_f32 v[10:11], v[10:11], v[20:21]
	s_nop 0
	v_pk_mul_f32 v[10:11], v[14:15], v[10:11]
	v_med3_f32 v14, v16, s72, v154
	v_med3_f32 v15, v17, s72, v154
	v_pk_mul_f32 v[16:17], v[12:13], s[88:89] op_sel_hi:[1,0]
	v_pk_add_f32 v[14:15], v[14:15], 1.0 op_sel_hi:[1,0]
	v_exp_f32_e32 v16, v16
	v_exp_f32_e32 v17, v17
	s_nop 0
	s_nop 0
	v_cvt_pk_fp8_f32 v20, v10, v11
	v_pk_add_f32 v[16:17], v[16:17], 1.0 op_sel_hi:[1,0]
	s_nop 0
	v_rcp_f32_e32 v16, v16
	v_rcp_f32_e32 v17, v17
	s_nop 0
	v_pk_mul_f32 v[12:13], v[12:13], v[16:17]
	s_nop 0
	v_pk_mul_f32 v[12:13], v[14:15], v[12:13]
	v_pk_mul_f32 v[14:15], v[2:3], s[88:89] op_sel_hi:[1,0]
	v_cvt_pk_fp8_f32 v20, v12, v13 op_sel:[0,0,1]
	v_exp_f32_e32 v14, v14
	v_exp_f32_e32 v15, v15
	s_nop 1
	v_permlane16_swap_b32 v18, v20
	s_nop 0
	v_pk_add_f32 v[14:15], v[14:15], 1.0 op_sel_hi:[1,0]
	s_nop 0
	v_rcp_f32_e32 v14, v14
	v_rcp_f32_e32 v15, v15
	s_nop 0
	v_pk_mul_f32 v[2:3], v[2:3], v[14:15]
	s_nop 0
	v_pk_mul_f32 v[2:3], v[6:7], v[2:3]
	v_med3_f32 v6, v8, s72, v154
	v_med3_f32 v7, v9, s72, v154
	v_pk_mul_f32 v[8:9], v[4:5], s[88:89] op_sel_hi:[1,0]
	v_cvt_pk_fp8_f32 v21, v2, v3
	v_exp_f32_e32 v8, v8
	v_exp_f32_e32 v9, v9
	v_pk_add_f32 v[6:7], v[6:7], 1.0 op_sel_hi:[1,0]
	v_pk_add_f32 v[8:9], v[8:9], 1.0 op_sel_hi:[1,0]
	s_nop 0
	v_rcp_f32_e32 v8, v8
	v_rcp_f32_e32 v9, v9
	s_nop 0
	v_pk_mul_f32 v[4:5], v[4:5], v[8:9]
	s_nop 0
	v_pk_mul_f32 v[4:5], v[6:7], v[4:5]
	s_nop 0
	v_cvt_pk_fp8_f32 v21, v4, v5 op_sel:[0,0,1]
	s_nop 0
	s_nop 1
	v_permlane16_swap_b32 v19, v21
	global_store_dwordx4 v0, v[18:21], s[8:9]
	s_cbranch_vccnz .LBB0_1784
	s_add_i32 s16, s58, 0x800
	s_cmpk_lg_i32 s58, 0x1000
	s_cselect_b32 s20, s16, 0
	s_andn2_b64 vcc, exec, s[6:7]
	s_cbranch_vccnz .LBB0_1783
	s_barrier
	s_branch .LBB0_1783

.LBB0_1875:
	v_add_u32_e32 v2, s63, v192
	ds_read_b128 v[14:17], v2
	ds_read_b128 v[10:13], v2 offset:16
	ds_read_b128 v[6:9], v2 offset:512
	ds_read_b128 v[2:5], v2 offset:528
	s_nop 0
	s_waitcnt lgkmcnt(0)
	v_pk_add_f32 v[22:23], v[158:159], v[14:15]
	v_pk_add_f32 v[26:27], v[154:155], v[10:11]
	v_cvt_pk_fp8_f32 v18, v22, v23
	v_cvt_pk_fp8_f32 v19, v26, v27
	v_pk_add_f32 v[20:21], v[160:161], v[16:17]
	v_pk_add_f32 v[24:25], v[156:157], v[12:13]
	v_cvt_pk_fp8_f32 v18, v20, v21 op_sel:[0,0,1]
	v_cvt_pk_fp8_f32 v19, v24, v25 op_sel:[0,0,1]
	v_pk_add_f32 v[24:25], v[150:151], v[14:15]
	v_pk_add_f32 v[28:29], v[146:147], v[10:11]
	v_cvt_pk_fp8_f32 v20, v24, v25
	v_cvt_pk_fp8_f32 v21, v28, v29
	v_pk_add_f32 v[22:23], v[152:153], v[16:17]
	v_pk_add_f32 v[26:27], v[148:149], v[12:13]
	v_lshl_or_b32 v30, s66, 8, v190
	v_lshl_add_u32 v31, s67, 18, v191
	v_cvt_pk_fp8_f32 v20, v22, v23 op_sel:[0,0,1]
	v_cvt_pk_fp8_f32 v21, v26, v27 op_sel:[0,0,1]
	v_or_b32_e32 v32, v31, v30
	s_nop 1
	v_permlane16_swap_b32 v18, v20
	s_nop 1
	v_permlane16_swap_b32 v19, v21
	global_store_dwordx4 v32, v[18:21], s[8:9]
	v_pk_add_f32 v[22:23], v[142:143], v[6:7]
	v_pk_add_f32 v[26:27], v[138:139], v[2:3]
	s_nop 0
	s_nop 0
	v_cvt_pk_fp8_f32 v18, v22, v23
	v_cvt_pk_fp8_f32 v19, v26, v27
	v_pk_add_f32 v[20:21], v[144:145], v[8:9]
	v_pk_add_f32 v[24:25], v[140:141], v[4:5]
	v_cvt_pk_fp8_f32 v18, v20, v21 op_sel:[0,0,1]
	v_cvt_pk_fp8_f32 v19, v24, v25 op_sel:[0,0,1]
	v_pk_add_f32 v[24:25], v[134:135], v[6:7]
	v_pk_add_f32 v[28:29], v[130:131], v[2:3]
	v_cvt_pk_fp8_f32 v20, v24, v25
	v_cvt_pk_fp8_f32 v21, v28, v29
	v_pk_add_f32 v[22:23], v[136:137], v[8:9]
	v_pk_add_f32 v[26:27], v[132:133], v[4:5]
	v_cvt_pk_fp8_f32 v20, v22, v23 op_sel:[0,0,1]
	v_cvt_pk_fp8_f32 v21, v26, v27 op_sel:[0,0,1]
	s_nop 1
	v_permlane16_swap_b32 v18, v20
	v_or_b32_e32 v22, 0x80, v32
	s_nop 1
	v_permlane16_swap_b32 v19, v21
	global_store_dwordx4 v22, v[18:21], s[8:9]
	v_pk_add_f32 v[22:23], v[126:127], v[14:15]
	v_pk_add_f32 v[26:27], v[122:123], v[10:11]
	s_nop 0
	s_nop 0
	v_cvt_pk_fp8_f32 v18, v22, v23
	v_cvt_pk_fp8_f32 v19, v26, v27
	v_pk_add_f32 v[20:21], v[128:129], v[16:17]
	v_pk_add_f32 v[24:25], v[124:125], v[12:13]
	v_cvt_pk_fp8_f32 v18, v20, v21 op_sel:[0,0,1]
	v_cvt_pk_fp8_f32 v19, v24, v25 op_sel:[0,0,1]
	v_pk_add_f32 v[24:25], v[118:119], v[14:15]
	v_pk_add_f32 v[28:29], v[114:115], v[10:11]
	v_cvt_pk_fp8_f32 v20, v24, v25
	v_cvt_pk_fp8_f32 v21, v28, v29
	v_pk_add_f32 v[22:23], v[120:121], v[16:17]
	v_pk_add_f32 v[26:27], v[116:117], v[12:13]
	v_cvt_pk_fp8_f32 v20, v22, v23 op_sel:[0,0,1]
	v_cvt_pk_fp8_f32 v21, v26, v27 op_sel:[0,0,1]
	v_or_b32_e32 v33, 0x8000, v32
	s_nop 1
	v_permlane16_swap_b32 v18, v20
	s_nop 1
	v_permlane16_swap_b32 v19, v21
	global_store_dwordx4 v33, v[18:21], s[8:9]
	v_pk_add_f32 v[22:23], v[110:111], v[6:7]
	v_pk_add_f32 v[26:27], v[106:107], v[2:3]
	s_nop 0
	s_nop 0
	v_cvt_pk_fp8_f32 v18, v22, v23
	v_cvt_pk_fp8_f32 v19, v26, v27
	v_pk_add_f32 v[20:21], v[112:113], v[8:9]
	v_pk_add_f32 v[24:25], v[108:109], v[4:5]
	v_cvt_pk_fp8_f32 v18, v20, v21 op_sel:[0,0,1]
	v_cvt_pk_fp8_f32 v19, v24, v25 op_sel:[0,0,1]
	v_pk_add_f32 v[24:25], v[102:103], v[6:7]
	v_pk_add_f32 v[28:29], v[98:99], v[2:3]
	v_cvt_pk_fp8_f32 v20, v24, v25
	v_cvt_pk_fp8_f32 v21, v28, v29
	v_pk_add_f32 v[22:23], v[104:105], v[8:9]
	v_pk_add_f32 v[26:27], v[100:101], v[4:5]
	v_cvt_pk_fp8_f32 v20, v22, v23 op_sel:[0,0,1]
	v_cvt_pk_fp8_f32 v21, v26, v27 op_sel:[0,0,1]
	s_nop 1
	v_permlane16_swap_b32 v18, v20
	v_or_b32_e32 v22, 0x8080, v32
	s_nop 1
	v_permlane16_swap_b32 v19, v21
	global_store_dwordx4 v22, v[18:21], s[8:9]
	v_pk_add_f32 v[22:23], v[94:95], v[14:15]
	v_pk_add_f32 v[26:27], v[90:91], v[10:11]
	s_nop 0
	s_nop 0
	v_cvt_pk_fp8_f32 v18, v22, v23
	v_cvt_pk_fp8_f32 v19, v26, v27
	v_pk_add_f32 v[20:21], v[96:97], v[16:17]
	v_pk_add_f32 v[24:25], v[92:93], v[12:13]
	v_cvt_pk_fp8_f32 v18, v20, v21 op_sel:[0,0,1]
	v_cvt_pk_fp8_f32 v19, v24, v25 op_sel:[0,0,1]
	v_pk_add_f32 v[24:25], v[86:87], v[14:15]
	v_pk_add_f32 v[28:29], v[82:83], v[10:11]
	v_cvt_pk_fp8_f32 v20, v24, v25
	v_cvt_pk_fp8_f32 v21, v28, v29
	v_pk_add_f32 v[22:23], v[88:89], v[16:17]
	v_pk_add_f32 v[26:27], v[84:85], v[12:13]
	v_add_u32_e32 v30, v31, v30
	v_cvt_pk_fp8_f32 v20, v22, v23 op_sel:[0,0,1]
	v_cvt_pk_fp8_f32 v21, v26, v27 op_sel:[0,0,1]
	v_add_u32_e32 v31, 0x20000, v30
	s_nop 1
	v_permlane16_swap_b32 v18, v20
	s_nop 1
	v_permlane16_swap_b32 v19, v21
	global_store_dwordx4 v31, v[18:21], s[8:9]
	v_pk_add_f32 v[22:23], v[78:79], v[6:7]
	v_pk_add_f32 v[26:27], v[74:75], v[2:3]
	s_nop 0
	s_nop 0
	v_cvt_pk_fp8_f32 v18, v22, v23
	v_cvt_pk_fp8_f32 v19, v26, v27
	v_pk_add_f32 v[20:21], v[80:81], v[8:9]
	v_pk_add_f32 v[24:25], v[76:77], v[4:5]
	v_cvt_pk_fp8_f32 v18, v20, v21 op_sel:[0,0,1]
	v_cvt_pk_fp8_f32 v19, v24, v25 op_sel:[0,0,1]
	v_pk_add_f32 v[24:25], v[70:71], v[6:7]
	v_pk_add_f32 v[28:29], v[66:67], v[2:3]
	v_cvt_pk_fp8_f32 v20, v24, v25
	v_cvt_pk_fp8_f32 v21, v28, v29
	v_pk_add_f32 v[22:23], v[72:73], v[8:9]
	v_pk_add_f32 v[26:27], v[68:69], v[4:5]
	v_cvt_pk_fp8_f32 v20, v22, v23 op_sel:[0,0,1]
	v_cvt_pk_fp8_f32 v21, v26, v27 op_sel:[0,0,1]
	s_nop 1
	v_permlane16_swap_b32 v18, v20
	v_add_u32_e32 v22, 0x20080, v30
	s_nop 1
	v_permlane16_swap_b32 v19, v21
	global_store_dwordx4 v22, v[18:21], s[8:9]
	v_pk_add_f32 v[22:23], v[62:63], v[14:15]
	v_pk_add_f32 v[26:27], v[58:59], v[10:11]
	s_nop 0
	v_cvt_pk_fp8_f32 v18, v22, v23
	v_pk_add_f32 v[20:21], v[64:65], v[16:17]
	v_pk_add_f32 v[14:15], v[54:55], v[14:15]
	v_cvt_pk_fp8_f32 v18, v20, v21 op_sel:[0,0,1]
	v_pk_add_f32 v[10:11], v[50:51], v[10:11]
	v_cvt_pk_fp8_f32 v19, v26, v27
	v_cvt_pk_fp8_f32 v20, v14, v15
	v_cvt_pk_fp8_f32 v21, v10, v11
	v_pk_add_f32 v[14:15], v[46:47], v[6:7]
	v_cvt_pk_fp8_f32 v10, v14, v15
	v_pk_add_f32 v[24:25], v[60:61], v[12:13]
	v_pk_add_f32 v[16:17], v[56:57], v[16:17]
	v_pk_add_f32 v[12:13], v[52:53], v[12:13]
	v_cvt_pk_fp8_f32 v19, v24, v25 op_sel:[0,0,1]
	v_cvt_pk_fp8_f32 v20, v16, v17 op_sel:[0,0,1]
	v_cvt_pk_fp8_f32 v21, v12, v13 op_sel:[0,0,1]
	v_add_u32_e32 v28, 0x28000, v30
	s_nop 1
	v_permlane16_swap_b32 v18, v20
	s_nop 1
	v_permlane16_swap_b32 v19, v21
	v_pk_add_f32 v[12:13], v[48:49], v[8:9]
	global_store_dwordx4 v28, v[18:21], s[8:9]
	v_cvt_pk_fp8_f32 v10, v12, v13 op_sel:[0,0,1]
	s_nop 0
	v_pk_add_f32 v[18:19], v[42:43], v[2:3]
	v_pk_add_f32 v[6:7], v[38:39], v[6:7]
	v_pk_add_f32 v[2:3], v[34:35], v[2:3]
	v_cvt_pk_fp8_f32 v11, v18, v19
	v_cvt_pk_fp8_f32 v12, v6, v7
	v_cvt_pk_fp8_f32 v13, v2, v3
	v_pk_add_f32 v[16:17], v[44:45], v[4:5]
	v_pk_add_f32 v[8:9], v[40:41], v[8:9]
	v_pk_add_f32 v[4:5], v[36:37], v[4:5]
	v_cvt_pk_fp8_f32 v11, v16, v17 op_sel:[0,0,1]
	v_cvt_pk_fp8_f32 v12, v8, v9 op_sel:[0,0,1]
	v_cvt_pk_fp8_f32 v13, v4, v5 op_sel:[0,0,1]
	v_add_u32_e32 v2, 0x28080, v30
	s_mov_b64 s[18:19], -1
	s_and_b64 vcc, exec, s[4:5]
	s_nop 1
	v_permlane16_swap_b32 v10, v12
	s_nop 1
	v_permlane16_swap_b32 v11, v13
	global_store_dwordx4 v2, v[10:13], s[8:9]
	s_cbranch_vccnz .LBB0_1866
	s_add_i32 s4, s61, 0x800
	s_cmpk_lg_i32 s61, 0x1000
	s_cselect_b32 s4, s4, 0
	s_andn2_b64 vcc, exec, s[6:7]
	s_cbranch_vccnz .LBB0_1865
	s_barrier
	s_branch .LBB0_1865
